# strategy 1 (waitcnt placement) in the GEMM K-loops: the second s_waitcnt lgkmcnt(0) after each pre-MFMA barrier deleted (the counter is already zero before the barrier)
# baseline (speedup 1.0000x reference)
.LBB0_177:
	s_waitcnt vmcnt(8)
	s_add_u32 s2, s56, 0x80
	s_waitcnt lgkmcnt(0)
	s_addc_u32 s12, s57, 0
	s_and_b64 s[4:5], s[4:5], exec
	s_cselect_b32 s5, s43, s12
	s_cselect_b32 s4, s42, s2
	s_cselect_b32 s59, s53, s81
	s_cselect_b32 s58, s77, s80
	s_barrier
	s_setprio 1
	s_waitcnt lgkmcnt(0)
	v_mfma_scale_f32_16x16x128_f8f6f4 v[188:191], v[16:23], v[56:63], v[188:191], v230, v231 op_sel_hi:[0,0,0]
	v_mfma_scale_f32_16x16x128_f8f6f4 v[184:187], v[24:31], v[56:63], v[184:187], v230, v231 op_sel_hi:[0,0,0]
	v_mfma_scale_f32_16x16x128_f8f6f4 v[180:183], v[16:23], v[48:55], v[180:183], v230, v231 op_sel_hi:[0,0,0]
	v_mfma_scale_f32_16x16x128_f8f6f4 v[176:179], v[24:31], v[48:55], v[176:179], v230, v231 op_sel_hi:[0,0,0]
	v_mfma_scale_f32_16x16x128_f8f6f4 v[164:167], v[16:23], v[40:47], v[164:167], v230, v231 op_sel_hi:[0,0,0]
	v_mfma_scale_f32_16x16x128_f8f6f4 v[160:163], v[24:31], v[40:47], v[160:163], v230, v231 op_sel_hi:[0,0,0]
	v_mfma_scale_f32_16x16x128_f8f6f4 v[148:151], v[16:23], v[32:39], v[148:151], v230, v231 op_sel_hi:[0,0,0]
	v_mfma_scale_f32_16x16x128_f8f6f4 v[144:147], v[24:31], v[32:39], v[144:147], v230, v231 op_sel_hi:[0,0,0]
	s_setprio 0
	s_setprio 1
	v_mfma_scale_f32_16x16x128_f8f6f4 v[172:175], v[0:7], v[56:63], v[172:175], v230, v231 op_sel_hi:[0,0,0]
	v_mfma_scale_f32_16x16x128_f8f6f4 v[168:171], v[8:15], v[56:63], v[168:171], v230, v231 op_sel_hi:[0,0,0]
	v_mfma_scale_f32_16x16x128_f8f6f4 v[156:159], v[0:7], v[48:55], v[156:159], v230, v231 op_sel_hi:[0,0,0]
	v_mfma_scale_f32_16x16x128_f8f6f4 v[152:155], v[8:15], v[48:55], v[152:155], v230, v231 op_sel_hi:[0,0,0]
	v_mfma_scale_f32_16x16x128_f8f6f4 v[140:143], v[0:7], v[40:47], v[140:143], v230, v231 op_sel_hi:[0,0,0]
	v_mfma_scale_f32_16x16x128_f8f6f4 v[136:139], v[8:15], v[40:47], v[136:139], v230, v231 op_sel_hi:[0,0,0]
	v_mfma_scale_f32_16x16x128_f8f6f4 v[132:135], v[0:7], v[32:39], v[132:135], v230, v231 op_sel_hi:[0,0,0]
	v_mfma_scale_f32_16x16x128_f8f6f4 v[128:131], v[8:15], v[32:39], v[128:131], v230, v231 op_sel_hi:[0,0,0]
	s_setprio 0
	s_barrier
	s_mov_b32 m0, s63
	v_lshl_add_u64 v[226:227], s[58:59], 0, v[204:205]
	s_add_u32 s86, s58, 0x20000
	ds_read_b128 v[32:35], v237 offset:16384
	ds_read_b128 v[36:39], v237 offset:17408
	ds_read_b128 v[40:43], v237 offset:18432
	ds_read_b128 v[44:47], v237 offset:19456
	ds_read_b128 v[48:51], v237 offset:20480
	ds_read_b128 v[52:55], v237 offset:21504
	ds_read_b128 v[56:59], v237 offset:22528
	ds_read_b128 v[60:63], v237 offset:23552
	global_load_lds_dwordx4 v[226:227], off
	v_lshl_add_u64 v[228:229], s[58:59], 0, v[202:203]
	s_mov_b32 m0, s64
	s_addc_u32 s87, s59, 0
	global_load_lds_dwordx4 v[228:229], off
	v_lshl_add_u64 v[240:241], s[86:87], 0, v[204:205]
	s_mov_b32 m0, s65
	v_mov_b32_e32 v211, v193
	global_load_lds_dwordx4 v[240:241], off
	v_lshl_add_u64 v[240:241], s[86:87], 0, v[202:203]
	s_mov_b32 m0, s66
	v_lshl_add_u64 v[242:243], s[4:5], 0, v[210:211]
	global_load_lds_dwordx4 v[240:241], off
	s_mov_b32 m0, s62
	v_lshl_add_u64 v[240:241], s[4:5], 0, v[192:193]
	global_load_lds_dwordx4 v192, s[4:5]
	s_mov_b32 m0, s67
	s_nop 0
	global_load_lds_dwordx4 v210, s[4:5]
	s_waitcnt vmcnt(8)
	s_waitcnt lgkmcnt(0)
	s_barrier
	s_setprio 1
	v_mfma_scale_f32_16x16x128_f8f6f4 v[124:127], v[16:23], v[32:39], v[124:127], v230, v231 op_sel_hi:[0,0,0]
	v_mfma_scale_f32_16x16x128_f8f6f4 v[120:123], v[24:31], v[32:39], v[120:123], v230, v231 op_sel_hi:[0,0,0]
	v_mfma_scale_f32_16x16x128_f8f6f4 v[116:119], v[16:23], v[40:47], v[116:119], v230, v231 op_sel_hi:[0,0,0]
	v_mfma_scale_f32_16x16x128_f8f6f4 v[112:115], v[24:31], v[40:47], v[112:115], v230, v231 op_sel_hi:[0,0,0]
	v_mfma_scale_f32_16x16x128_f8f6f4 v[100:103], v[16:23], v[48:55], v[100:103], v230, v231 op_sel_hi:[0,0,0]
	v_mfma_scale_f32_16x16x128_f8f6f4 v[96:99], v[24:31], v[48:55], v[96:99], v230, v231 op_sel_hi:[0,0,0]
	v_mfma_scale_f32_16x16x128_f8f6f4 v[84:87], v[16:23], v[56:63], v[84:87], v230, v231 op_sel_hi:[0,0,0]
	v_mfma_scale_f32_16x16x128_f8f6f4 v[80:83], v[24:31], v[56:63], v[80:83], v230, v231 op_sel_hi:[0,0,0]
	s_setprio 0
	s_setprio 1
	v_mfma_scale_f32_16x16x128_f8f6f4 v[108:111], v[0:7], v[32:39], v[108:111], v230, v231 op_sel_hi:[0,0,0]
	v_mfma_scale_f32_16x16x128_f8f6f4 v[104:107], v[8:15], v[32:39], v[104:107], v230, v231 op_sel_hi:[0,0,0]
	v_mfma_scale_f32_16x16x128_f8f6f4 v[92:95], v[0:7], v[40:47], v[92:95], v230, v231 op_sel_hi:[0,0,0]
	v_mfma_scale_f32_16x16x128_f8f6f4 v[88:91], v[8:15], v[40:47], v[88:91], v230, v231 op_sel_hi:[0,0,0]
	v_mfma_scale_f32_16x16x128_f8f6f4 v[76:79], v[0:7], v[48:55], v[76:79], v230, v231 op_sel_hi:[0,0,0]
	v_mfma_scale_f32_16x16x128_f8f6f4 v[72:75], v[8:15], v[48:55], v[72:75], v230, v231 op_sel_hi:[0,0,0]
	v_mfma_scale_f32_16x16x128_f8f6f4 v[68:71], v[0:7], v[56:63], v[68:71], v230, v231 op_sel_hi:[0,0,0]
	v_mfma_scale_f32_16x16x128_f8f6f4 v[64:67], v[8:15], v[56:63], v[64:67], v230, v231 op_sel_hi:[0,0,0]
	s_setprio 0
	s_barrier
	s_add_i32 s2, 0, 0x18000
	s_add_i32 s12, 0, 0x1c000
	v_add_u32_e32 v12, s2, v236
	v_add_u32_e32 v28, s12, v236
	ds_read_b128 v[0:3], v12
	ds_read_b128 v[4:7], v12 offset:1024
	ds_read_b128 v[8:11], v12 offset:2048
	ds_read_b128 v[12:15], v12 offset:3072
	ds_read_b128 v[16:19], v28
	ds_read_b128 v[20:23], v28 offset:1024
	ds_read_b128 v[24:27], v28 offset:2048
	ds_read_b128 v[28:31], v28 offset:3072
	s_mov_b32 m0, s68
	v_lshl_add_u64 v[220:221], s[4:5], 0, v[220:221]
	ds_read_b128 v[32:35], v237 offset:32768
	ds_read_b128 v[36:39], v237 offset:33792
	ds_read_b128 v[40:43], v237 offset:34816
	ds_read_b128 v[44:47], v237 offset:35840
	ds_read_b128 v[48:51], v237 offset:36864
	ds_read_b128 v[52:55], v237 offset:37888
	ds_read_b128 v[56:59], v237 offset:38912
	ds_read_b128 v[60:63], v237 offset:39936
	global_load_lds_dwordx4 v[220:221], off
	v_lshl_add_u64 v[218:219], s[4:5], 0, v[218:219]
	s_mov_b32 m0, s69
	s_nop 0
	global_load_lds_dwordx4 v[218:219], off
	s_waitcnt vmcnt(8)
	s_waitcnt lgkmcnt(0)
	s_barrier
	s_setprio 1
	v_mfma_scale_f32_16x16x128_f8f6f4 v[188:191], v[0:7], v[32:39], v[188:191], v230, v231 op_sel_hi:[0,0,0]
	v_mfma_scale_f32_16x16x128_f8f6f4 v[184:187], v[8:15], v[32:39], v[184:187], v230, v231 op_sel_hi:[0,0,0]
	v_mfma_scale_f32_16x16x128_f8f6f4 v[180:183], v[0:7], v[40:47], v[180:183], v230, v231 op_sel_hi:[0,0,0]
	v_mfma_scale_f32_16x16x128_f8f6f4 v[176:179], v[8:15], v[40:47], v[176:179], v230, v231 op_sel_hi:[0,0,0]
	v_mfma_scale_f32_16x16x128_f8f6f4 v[164:167], v[0:7], v[48:55], v[164:167], v230, v231 op_sel_hi:[0,0,0]
	v_mfma_scale_f32_16x16x128_f8f6f4 v[160:163], v[8:15], v[48:55], v[160:163], v230, v231 op_sel_hi:[0,0,0]
	v_mfma_scale_f32_16x16x128_f8f6f4 v[148:151], v[0:7], v[56:63], v[148:151], v230, v231 op_sel_hi:[0,0,0]
	v_mfma_scale_f32_16x16x128_f8f6f4 v[144:147], v[8:15], v[56:63], v[144:147], v230, v231 op_sel_hi:[0,0,0]
	s_setprio 0
	s_setprio 1
	v_mfma_scale_f32_16x16x128_f8f6f4 v[172:175], v[16:23], v[32:39], v[172:175], v230, v231 op_sel_hi:[0,0,0]
	v_mfma_scale_f32_16x16x128_f8f6f4 v[168:171], v[24:31], v[32:39], v[168:171], v230, v231 op_sel_hi:[0,0,0]
	v_mfma_scale_f32_16x16x128_f8f6f4 v[156:159], v[16:23], v[40:47], v[156:159], v230, v231 op_sel_hi:[0,0,0]
	v_mfma_scale_f32_16x16x128_f8f6f4 v[152:155], v[24:31], v[40:47], v[152:155], v230, v231 op_sel_hi:[0,0,0]
	v_mfma_scale_f32_16x16x128_f8f6f4 v[140:143], v[16:23], v[48:55], v[140:143], v230, v231 op_sel_hi:[0,0,0]
	v_mfma_scale_f32_16x16x128_f8f6f4 v[136:139], v[24:31], v[48:55], v[136:139], v230, v231 op_sel_hi:[0,0,0]
	v_mfma_scale_f32_16x16x128_f8f6f4 v[132:135], v[16:23], v[56:63], v[132:135], v230, v231 op_sel_hi:[0,0,0]
	v_mfma_scale_f32_16x16x128_f8f6f4 v[128:131], v[24:31], v[56:63], v[128:131], v230, v231 op_sel_hi:[0,0,0]
	s_setprio 0
	s_barrier
	s_add_i32 s2, s2, s23
	v_lshl_add_u64 v[218:219], v[226:227], 0, s[26:27]
	s_mov_b32 m0, s2
	ds_read_b128 v[32:35], v237 offset:49152
	ds_read_b128 v[36:39], v237 offset:50176
	ds_read_b128 v[40:43], v237 offset:51200
	ds_read_b128 v[44:47], v237 offset:52224
	ds_read_b128 v[48:51], v237 offset:53248
	ds_read_b128 v[52:55], v237 offset:54272
	ds_read_b128 v[56:59], v237 offset:55296
	ds_read_b128 v[60:63], v237 offset:56320
	global_load_lds_dwordx4 v[218:219], off
	s_add_i32 m0, s2, 0x2000
	s_add_u32 s4, s58, 0x20080
	v_lshl_add_u64 v[218:219], v[228:229], 0, s[26:27]
	s_addc_u32 s5, s59, 0
	s_add_i32 s2, s12, s23
	global_load_lds_dwordx4 v[218:219], off
	v_lshl_add_u64 v[218:219], s[4:5], 0, v[204:205]
	s_mov_b32 m0, s2
	s_nop 0
	global_load_lds_dwordx4 v[218:219], off
	v_lshl_add_u64 v[218:219], s[4:5], 0, v[202:203]
	s_add_i32 m0, s2, 0x2000
	s_nop 0
	global_load_lds_dwordx4 v[218:219], off
	v_lshl_add_u64 v[218:219], v[240:241], 0, s[26:27]
	s_mov_b32 m0, s72
	s_nop 0
	global_load_lds_dwordx4 v[218:219], off
	v_lshl_add_u64 v[218:219], v[242:243], 0, s[26:27]
	s_mov_b32 m0, s10
	s_nop 0
	global_load_lds_dwordx4 v[218:219], off
	s_waitcnt vmcnt(8)
	s_waitcnt lgkmcnt(0)
	s_barrier
	s_setprio 1
	v_mfma_scale_f32_16x16x128_f8f6f4 v[124:127], v[0:7], v[32:39], v[124:127], v230, v231 op_sel_hi:[0,0,0]
	v_mfma_scale_f32_16x16x128_f8f6f4 v[120:123], v[8:15], v[32:39], v[120:123], v230, v231 op_sel_hi:[0,0,0]
	v_mfma_scale_f32_16x16x128_f8f6f4 v[116:119], v[0:7], v[40:47], v[116:119], v230, v231 op_sel_hi:[0,0,0]
	v_mfma_scale_f32_16x16x128_f8f6f4 v[112:115], v[8:15], v[40:47], v[112:115], v230, v231 op_sel_hi:[0,0,0]
	v_mfma_scale_f32_16x16x128_f8f6f4 v[100:103], v[0:7], v[48:55], v[100:103], v230, v231 op_sel_hi:[0,0,0]
	v_mfma_scale_f32_16x16x128_f8f6f4 v[96:99], v[8:15], v[48:55], v[96:99], v230, v231 op_sel_hi:[0,0,0]
	v_mfma_scale_f32_16x16x128_f8f6f4 v[84:87], v[0:7], v[56:63], v[84:87], v230, v231 op_sel_hi:[0,0,0]
	v_mfma_scale_f32_16x16x128_f8f6f4 v[80:83], v[8:15], v[56:63], v[80:83], v230, v231 op_sel_hi:[0,0,0]
	s_setprio 0
	s_setprio 1
	v_mfma_scale_f32_16x16x128_f8f6f4 v[108:111], v[16:23], v[32:39], v[108:111], v230, v231 op_sel_hi:[0,0,0]
	v_mfma_scale_f32_16x16x128_f8f6f4 v[104:107], v[24:31], v[32:39], v[104:107], v230, v231 op_sel_hi:[0,0,0]
	v_mfma_scale_f32_16x16x128_f8f6f4 v[92:95], v[16:23], v[40:47], v[92:95], v230, v231 op_sel_hi:[0,0,0]
	v_mfma_scale_f32_16x16x128_f8f6f4 v[88:91], v[24:31], v[40:47], v[88:91], v230, v231 op_sel_hi:[0,0,0]
	v_mfma_scale_f32_16x16x128_f8f6f4 v[76:79], v[16:23], v[48:55], v[76:79], v230, v231 op_sel_hi:[0,0,0]
	v_mfma_scale_f32_16x16x128_f8f6f4 v[72:75], v[24:31], v[48:55], v[72:75], v230, v231 op_sel_hi:[0,0,0]
	v_mfma_scale_f32_16x16x128_f8f6f4 v[68:71], v[16:23], v[56:63], v[68:71], v230, v231 op_sel_hi:[0,0,0]
	v_mfma_scale_f32_16x16x128_f8f6f4 v[64:67], v[24:31], v[56:63], v[64:67], v230, v231 op_sel_hi:[0,0,0]
	s_setprio 0
	s_barrier
	s_add_i32 s82, s82, 2
	s_add_u32 s56, s56, 0x100
	s_addc_u32 s57, s57, 0
	s_add_u32 s80, s80, 0x100
	s_addc_u32 s81, s81, 0
	s_cmp_gt_u32 s82, 5
	s_cbranch_scc1 .LBB0_180

.LBB0_486:
	s_ashr_i32 s49, s48, 31
	s_lshl_b64 s[50:51], s[48:49], 17
	s_add_u32 s50, s7, s50
	s_addc_u32 s51, s8, s51
	s_and_b64 s[52:53], s[36:37], exec
	s_cselect_b32 s59, s51, s61
	s_cselect_b32 s58, s50, s60
	s_ashr_i32 s47, s46, 31
	s_lshl_b64 s[52:53], s[46:47], 17
	s_add_u32 s52, s9, s52
	s_addc_u32 s53, s10, s53
	s_and_b64 s[56:57], s[36:37], exec
	s_cselect_b32 s57, s53, s55
	s_cselect_b32 s56, s52, s54
	s_add_i32 s65, 0, 0x10000
	s_add_i32 s49, 0, 0x14000
	v_add_u32_e32 v194, s65, v138
	v_add_u32_e32 v195, s49, v138
	ds_read_b128 v[4:7], v194
	ds_read_b128 v[8:11], v194 offset:1024
	ds_read_b128 v[12:15], v194 offset:2048
	ds_read_b128 v[16:19], v194 offset:3072
	ds_read_b128 v[20:23], v195
	ds_read_b128 v[24:27], v195 offset:1024
	ds_read_b128 v[28:31], v195 offset:2048
	ds_read_b128 v[32:35], v195 offset:3072
	v_lshl_add_u64 v[0:1], s[60:61], 0, v[136:137]
	s_add_i32 s64, s19, 0xc000
	v_lshl_add_u64 v[2:3], v[0:1], 0, s[26:27]
	s_mov_b32 m0, s64
	ds_read_b128 v[36:39], v139
	ds_read_b128 v[40:43], v139 offset:1024
	ds_read_b128 v[44:47], v139 offset:2048
	ds_read_b128 v[48:51], v139 offset:3072
	ds_read_b128 v[52:55], v139 offset:4096
	ds_read_b128 v[56:59], v139 offset:5120
	ds_read_b128 v[60:63], v139 offset:6144
	ds_read_b128 v[64:67], v139 offset:7168
	global_load_lds_dwordx4 v[2:3], off
	v_lshl_add_u64 v[2:3], s[60:61], 0, v[132:133]
	s_add_i32 s2, s19, 0xe000
	v_lshl_add_u64 v[68:69], v[2:3], 0, s[26:27]
	s_mov_b32 m0, s2
	s_nop 0
	global_load_lds_dwordx4 v[68:69], off
	s_waitcnt vmcnt(8)
	s_waitcnt lgkmcnt(0)
	s_barrier
	s_setprio 1
	v_mfma_f32_16x16x32_bf16 v[68:71], v[4:7], v[36:39], 0
	v_mfma_f32_16x16x32_bf16 v[72:75], v[12:15], v[36:39], 0
	v_mfma_f32_16x16x32_bf16 v[76:79], v[4:7], v[44:47], 0
	v_mfma_f32_16x16x32_bf16 v[80:83], v[12:15], v[44:47], 0
	v_mfma_f32_16x16x32_bf16 v[84:87], v[4:7], v[52:55], 0
	v_mfma_f32_16x16x32_bf16 v[88:91], v[12:15], v[52:55], 0
	v_mfma_f32_16x16x32_bf16 v[92:95], v[4:7], v[60:63], 0
	v_mfma_f32_16x16x32_bf16 v[96:99], v[12:15], v[60:63], 0
	v_mfma_f32_16x16x32_bf16 v[68:71], v[8:11], v[40:43], v[68:71]
	v_mfma_f32_16x16x32_bf16 v[72:75], v[16:19], v[40:43], v[72:75]
	v_mfma_f32_16x16x32_bf16 v[76:79], v[8:11], v[48:51], v[76:79]
	v_mfma_f32_16x16x32_bf16 v[80:83], v[16:19], v[48:51], v[80:83]
	v_mfma_f32_16x16x32_bf16 v[84:87], v[8:11], v[56:59], v[84:87]
	v_mfma_f32_16x16x32_bf16 v[88:91], v[16:19], v[56:59], v[88:91]
	v_mfma_f32_16x16x32_bf16 v[92:95], v[8:11], v[64:67], v[92:95]
	v_mfma_f32_16x16x32_bf16 v[96:99], v[16:19], v[64:67], v[96:99]
	s_setprio 0
	s_setprio 1
	v_mfma_f32_16x16x32_bf16 v[100:103], v[20:23], v[36:39], 0
	v_mfma_f32_16x16x32_bf16 v[36:39], v[28:31], v[36:39], 0
	v_mfma_f32_16x16x32_bf16 v[100:103], v[24:27], v[40:43], v[100:103]
	v_mfma_f32_16x16x32_bf16 v[36:39], v[32:35], v[40:43], v[36:39]
	v_mfma_f32_16x16x32_bf16 v[40:43], v[20:23], v[44:47], 0
	v_mfma_f32_16x16x32_bf16 v[44:47], v[28:31], v[44:47], 0
	v_mfma_f32_16x16x32_bf16 v[40:43], v[24:27], v[48:51], v[40:43]
	v_mfma_f32_16x16x32_bf16 v[44:47], v[32:35], v[48:51], v[44:47]
	v_mfma_f32_16x16x32_bf16 v[48:51], v[20:23], v[52:55], 0
	v_mfma_f32_16x16x32_bf16 v[52:55], v[28:31], v[52:55], 0
	v_mfma_f32_16x16x32_bf16 v[48:51], v[24:27], v[56:59], v[48:51]
	v_mfma_f32_16x16x32_bf16 v[52:55], v[32:35], v[56:59], v[52:55]
	v_mfma_f32_16x16x32_bf16 v[56:59], v[20:23], v[60:63], 0
	v_mfma_f32_16x16x32_bf16 v[60:63], v[28:31], v[60:63], 0
	v_mfma_f32_16x16x32_bf16 v[56:59], v[24:27], v[64:67], v[56:59]
	v_mfma_f32_16x16x32_bf16 v[60:63], v[32:35], v[64:67], v[60:63]
	s_setprio 0
	s_barrier
	s_add_i32 s65, s65, s17
	v_lshl_add_u64 v[218:219], s[54:55], 0, v[192:193]
	s_mov_b64 s[68:69], 0x100
	s_add_i32 s47, s65, 0x2000
	v_lshl_add_u64 v[144:145], v[218:219], 0, s[68:69]
	s_mov_b32 m0, s65
	v_lshl_add_u64 v[220:221], s[54:55], 0, v[128:129]
	s_add_u32 s66, s54, 0x10100
	ds_read_b128 v[64:67], v139 offset:16384
	ds_read_b128 v[104:107], v139 offset:17408
	ds_read_b128 v[108:111], v139 offset:18432
	ds_read_b128 v[112:115], v139 offset:19456
	ds_read_b128 v[116:119], v139 offset:20480
	ds_read_b128 v[120:123], v139 offset:21504
	ds_read_b128 v[124:127], v139 offset:22528
	ds_read_b128 v[140:143], v139 offset:23552
	global_load_lds_dwordx4 v[144:145], off
	v_lshl_add_u64 v[144:145], v[220:221], 0, s[68:69]
	s_mov_b32 m0, s47
	s_addc_u32 s67, s55, 0
	s_add_i32 s49, s49, s17
	global_load_lds_dwordx4 v[144:145], off
	v_lshl_add_u64 v[144:145], s[66:67], 0, v[192:193]
	s_mov_b32 m0, s49
	s_add_i32 s63, s49, 0x2000
	global_load_lds_dwordx4 v[144:145], off
	v_lshl_add_u64 v[144:145], s[66:67], 0, v[128:129]
	s_mov_b32 m0, s63
	v_lshl_add_u64 v[226:227], s[60:61], 0, v[134:135]
	global_load_lds_dwordx4 v[144:145], off
	v_lshl_add_u64 v[144:145], v[226:227], 0, s[68:69]
	s_mov_b32 m0, s19
	v_lshl_add_u64 v[228:229], s[60:61], 0, v[130:131]
	global_load_lds_dwordx4 v[144:145], off
	v_lshl_add_u64 v[144:145], v[228:229], 0, s[68:69]
	s_mov_b32 m0, s22
	s_nop 0
	global_load_lds_dwordx4 v[144:145], off
	s_waitcnt vmcnt(8)
	s_waitcnt lgkmcnt(0)
	s_barrier
	s_setprio 1
	v_mfma_f32_16x16x32_bf16 v[144:147], v[4:7], v[64:67], 0
	v_mfma_f32_16x16x32_bf16 v[152:155], v[4:7], v[108:111], 0
	v_mfma_f32_16x16x32_bf16 v[160:163], v[4:7], v[116:119], 0
	v_mfma_f32_16x16x32_bf16 v[4:7], v[4:7], v[124:127], 0
	v_mfma_f32_16x16x32_bf16 v[144:147], v[8:11], v[104:107], v[144:147]
	v_mfma_f32_16x16x32_bf16 v[152:155], v[8:11], v[112:115], v[152:155]
	v_mfma_f32_16x16x32_bf16 v[160:163], v[8:11], v[120:123], v[160:163]
	v_mfma_f32_16x16x32_bf16 v[4:7], v[8:11], v[140:143], v[4:7]
	v_mfma_f32_16x16x32_bf16 v[8:11], v[12:15], v[124:127], 0
	v_mfma_f32_16x16x32_bf16 v[148:151], v[12:15], v[64:67], 0
	v_mfma_f32_16x16x32_bf16 v[156:159], v[12:15], v[108:111], 0
	v_mfma_f32_16x16x32_bf16 v[164:167], v[12:15], v[116:119], 0
	v_mfma_f32_16x16x32_bf16 v[8:11], v[16:19], v[140:143], v[8:11]
	v_mfma_f32_16x16x32_bf16 v[148:151], v[16:19], v[104:107], v[148:151]
	v_mfma_f32_16x16x32_bf16 v[156:159], v[16:19], v[112:115], v[156:159]
	v_mfma_f32_16x16x32_bf16 v[164:167], v[16:19], v[120:123], v[164:167]
	s_setprio 0
	s_setprio 1
	v_mfma_f32_16x16x32_bf16 v[12:15], v[20:23], v[64:67], 0
	v_mfma_f32_16x16x32_bf16 v[16:19], v[28:31], v[64:67], 0
	v_mfma_f32_16x16x32_bf16 v[12:15], v[24:27], v[104:107], v[12:15]
	v_mfma_f32_16x16x32_bf16 v[16:19], v[32:35], v[104:107], v[16:19]
	v_mfma_f32_16x16x32_bf16 v[64:67], v[20:23], v[108:111], 0
	v_mfma_f32_16x16x32_bf16 v[104:107], v[28:31], v[108:111], 0
	v_mfma_f32_16x16x32_bf16 v[108:111], v[20:23], v[116:119], 0
	v_mfma_f32_16x16x32_bf16 v[20:23], v[20:23], v[124:127], 0
	v_mfma_f32_16x16x32_bf16 v[64:67], v[24:27], v[112:115], v[64:67]
	v_mfma_f32_16x16x32_bf16 v[104:107], v[32:35], v[112:115], v[104:107]
	v_mfma_f32_16x16x32_bf16 v[108:111], v[24:27], v[120:123], v[108:111]
	v_mfma_f32_16x16x32_bf16 v[112:115], v[28:31], v[116:119], 0
	v_mfma_f32_16x16x32_bf16 v[20:23], v[24:27], v[140:143], v[20:23]
	v_mfma_f32_16x16x32_bf16 v[24:27], v[28:31], v[124:127], 0
	v_mfma_f32_16x16x32_bf16 v[112:115], v[32:35], v[120:123], v[112:115]
	v_mfma_f32_16x16x32_bf16 v[24:27], v[32:35], v[140:143], v[24:27]
	s_setprio 0
	s_barrier
	s_add_i32 s61, 0, 0x18000
	s_add_i32 s12, 0, 0x1c000
	v_add_u32_e32 v232, s61, v138
	v_add_u32_e32 v234, s12, v138
	ds_read_b128 v[28:31], v232
	ds_read_b128 v[32:35], v232 offset:1024
	ds_read_b128 v[116:119], v232 offset:2048
	ds_read_b128 v[120:123], v232 offset:3072
	ds_read_b128 v[124:127], v234
	ds_read_b128 v[140:143], v234 offset:1024
	ds_read_b128 v[168:171], v234 offset:2048
	ds_read_b128 v[172:175], v234 offset:3072
	s_mov_b32 m0, s23
	v_lshl_add_u64 v[230:231], v[0:1], 0, s[68:69]
	ds_read_b128 v[176:179], v139 offset:32768
	ds_read_b128 v[180:183], v139 offset:33792
	ds_read_b128 v[184:187], v139 offset:34816
	ds_read_b128 v[188:191], v139 offset:35840
	ds_read_b128 v[202:205], v139 offset:36864
	ds_read_b128 v[206:209], v139 offset:37888
	ds_read_b128 v[210:213], v139 offset:38912
	ds_read_b128 v[214:217], v139 offset:39936
	global_load_lds_dwordx4 v[230:231], off
	v_lshl_add_u64 v[230:231], v[2:3], 0, s[68:69]
	s_mov_b32 m0, s24
	s_nop 0
	global_load_lds_dwordx4 v[230:231], off
	s_waitcnt vmcnt(8)
	s_waitcnt lgkmcnt(0)
	s_barrier
	s_setprio 1
	v_mfma_f32_16x16x32_bf16 v[68:71], v[28:31], v[176:179], v[68:71]
	v_mfma_f32_16x16x32_bf16 v[72:75], v[116:119], v[176:179], v[72:75]
	v_mfma_f32_16x16x32_bf16 v[76:79], v[28:31], v[184:187], v[76:79]
	v_mfma_f32_16x16x32_bf16 v[80:83], v[116:119], v[184:187], v[80:83]
	v_mfma_f32_16x16x32_bf16 v[84:87], v[28:31], v[202:205], v[84:87]
	v_mfma_f32_16x16x32_bf16 v[88:91], v[116:119], v[202:205], v[88:91]
	v_mfma_f32_16x16x32_bf16 v[92:95], v[28:31], v[210:213], v[92:95]
	v_mfma_f32_16x16x32_bf16 v[96:99], v[116:119], v[210:213], v[96:99]
	v_mfma_f32_16x16x32_bf16 v[68:71], v[32:35], v[180:183], v[68:71]
	v_mfma_f32_16x16x32_bf16 v[72:75], v[120:123], v[180:183], v[72:75]
	v_mfma_f32_16x16x32_bf16 v[76:79], v[32:35], v[188:191], v[76:79]
	v_mfma_f32_16x16x32_bf16 v[80:83], v[120:123], v[188:191], v[80:83]
	v_mfma_f32_16x16x32_bf16 v[84:87], v[32:35], v[206:209], v[84:87]
	v_mfma_f32_16x16x32_bf16 v[88:91], v[120:123], v[206:209], v[88:91]
	v_mfma_f32_16x16x32_bf16 v[92:95], v[32:35], v[214:217], v[92:95]
	v_mfma_f32_16x16x32_bf16 v[96:99], v[120:123], v[214:217], v[96:99]
	s_setprio 0
	s_setprio 1
	v_mfma_f32_16x16x32_bf16 v[100:103], v[124:127], v[176:179], v[100:103]
	v_mfma_f32_16x16x32_bf16 v[36:39], v[168:171], v[176:179], v[36:39]
	v_mfma_f32_16x16x32_bf16 v[40:43], v[124:127], v[184:187], v[40:43]
	v_mfma_f32_16x16x32_bf16 v[44:47], v[168:171], v[184:187], v[44:47]
	v_mfma_f32_16x16x32_bf16 v[48:51], v[124:127], v[202:205], v[48:51]
	v_mfma_f32_16x16x32_bf16 v[52:55], v[168:171], v[202:205], v[52:55]
	v_mfma_f32_16x16x32_bf16 v[56:59], v[124:127], v[210:213], v[56:59]
	v_mfma_f32_16x16x32_bf16 v[60:63], v[168:171], v[210:213], v[60:63]
	v_mfma_f32_16x16x32_bf16 v[100:103], v[140:143], v[180:183], v[100:103]
	v_mfma_f32_16x16x32_bf16 v[36:39], v[172:175], v[180:183], v[36:39]
	v_mfma_f32_16x16x32_bf16 v[40:43], v[140:143], v[188:191], v[40:43]
	v_mfma_f32_16x16x32_bf16 v[44:47], v[172:175], v[188:191], v[44:47]
	v_mfma_f32_16x16x32_bf16 v[48:51], v[140:143], v[206:209], v[48:51]
	v_mfma_f32_16x16x32_bf16 v[52:55], v[172:175], v[206:209], v[52:55]
	v_mfma_f32_16x16x32_bf16 v[56:59], v[140:143], v[214:217], v[56:59]
	v_mfma_f32_16x16x32_bf16 v[60:63], v[172:175], v[214:217], v[60:63]
	s_setprio 0
	s_barrier
	s_add_i32 s61, s61, s17
	s_mov_b64 s[68:69], 0x180
	s_add_i32 s60, s61, 0x2000
	v_lshl_add_u64 v[218:219], v[218:219], 0, s[68:69]
	s_mov_b32 m0, s61
	s_add_u32 s66, s54, 0x10180
	ds_read_b128 v[176:179], v139 offset:49152
	ds_read_b128 v[180:183], v139 offset:50176
	ds_read_b128 v[184:187], v139 offset:51200
	ds_read_b128 v[188:191], v139 offset:52224
	ds_read_b128 v[202:205], v139 offset:53248
	ds_read_b128 v[206:209], v139 offset:54272
	ds_read_b128 v[210:213], v139 offset:55296
	ds_read_b128 v[214:217], v139 offset:56320
	global_load_lds_dwordx4 v[218:219], off
	v_lshl_add_u64 v[218:219], v[220:221], 0, s[68:69]
	s_mov_b32 m0, s60
	s_addc_u32 s67, s55, 0
	s_add_i32 s54, s12, s17
	global_load_lds_dwordx4 v[218:219], off
	v_lshl_add_u64 v[218:219], s[66:67], 0, v[192:193]
	s_mov_b32 m0, s54
	s_add_i32 s55, s54, 0x2000
	global_load_lds_dwordx4 v[218:219], off
	v_lshl_add_u64 v[218:219], s[66:67], 0, v[128:129]
	s_mov_b32 m0, s55
	s_nop 0
	global_load_lds_dwordx4 v[218:219], off
	v_lshl_add_u64 v[218:219], v[226:227], 0, s[68:69]
	s_mov_b32 m0, s30
	s_nop 0
	global_load_lds_dwordx4 v[218:219], off
	v_lshl_add_u64 v[218:219], v[228:229], 0, s[68:69]
	s_mov_b32 m0, s31
	s_nop 0
	global_load_lds_dwordx4 v[218:219], off
	s_waitcnt vmcnt(8)
	s_waitcnt lgkmcnt(0)
	s_barrier
	s_setprio 1
	v_mfma_f32_16x16x32_bf16 v[4:7], v[28:31], v[210:213], v[4:7]
	v_mfma_f32_16x16x32_bf16 v[8:11], v[116:119], v[210:213], v[8:11]
	v_mfma_f32_16x16x32_bf16 v[144:147], v[28:31], v[176:179], v[144:147]
	v_mfma_f32_16x16x32_bf16 v[148:151], v[116:119], v[176:179], v[148:151]
	v_mfma_f32_16x16x32_bf16 v[152:155], v[28:31], v[184:187], v[152:155]
	v_mfma_f32_16x16x32_bf16 v[156:159], v[116:119], v[184:187], v[156:159]
	v_mfma_f32_16x16x32_bf16 v[160:163], v[28:31], v[202:205], v[160:163]
	v_mfma_f32_16x16x32_bf16 v[164:167], v[116:119], v[202:205], v[164:167]
	v_mfma_f32_16x16x32_bf16 v[4:7], v[32:35], v[214:217], v[4:7]
	v_mfma_f32_16x16x32_bf16 v[8:11], v[120:123], v[214:217], v[8:11]
	v_mfma_f32_16x16x32_bf16 v[144:147], v[32:35], v[180:183], v[144:147]
	v_mfma_f32_16x16x32_bf16 v[148:151], v[120:123], v[180:183], v[148:151]
	v_mfma_f32_16x16x32_bf16 v[152:155], v[32:35], v[188:191], v[152:155]
	v_mfma_f32_16x16x32_bf16 v[156:159], v[120:123], v[188:191], v[156:159]
	v_mfma_f32_16x16x32_bf16 v[160:163], v[32:35], v[206:209], v[160:163]
	v_mfma_f32_16x16x32_bf16 v[164:167], v[120:123], v[206:209], v[164:167]
	s_setprio 0
	s_setprio 1
	v_mfma_f32_16x16x32_bf16 v[12:15], v[124:127], v[176:179], v[12:15]
	v_mfma_f32_16x16x32_bf16 v[16:19], v[168:171], v[176:179], v[16:19]
	v_mfma_f32_16x16x32_bf16 v[28:31], v[124:127], v[184:187], v[64:67]
	v_mfma_f32_16x16x32_bf16 v[32:35], v[168:171], v[184:187], v[104:107]
	v_mfma_f32_16x16x32_bf16 v[64:67], v[124:127], v[202:205], v[108:111]
	v_mfma_f32_16x16x32_bf16 v[104:107], v[168:171], v[202:205], v[112:115]
	v_mfma_f32_16x16x32_bf16 v[20:23], v[124:127], v[210:213], v[20:23]
	v_mfma_f32_16x16x32_bf16 v[24:27], v[168:171], v[210:213], v[24:27]
	v_mfma_f32_16x16x32_bf16 v[12:15], v[140:143], v[180:183], v[12:15]
	v_mfma_f32_16x16x32_bf16 v[16:19], v[172:175], v[180:183], v[16:19]
	v_mfma_f32_16x16x32_bf16 v[28:31], v[140:143], v[188:191], v[28:31]
	v_mfma_f32_16x16x32_bf16 v[32:35], v[172:175], v[188:191], v[32:35]
	v_mfma_f32_16x16x32_bf16 v[64:67], v[140:143], v[206:209], v[64:67]
	v_mfma_f32_16x16x32_bf16 v[104:107], v[172:175], v[206:209], v[104:107]
	v_mfma_f32_16x16x32_bf16 v[20:23], v[140:143], v[214:217], v[20:23]
	v_mfma_f32_16x16x32_bf16 v[24:27], v[172:175], v[214:217], v[24:27]
	s_setprio 0
	s_barrier
	ds_read_b128 v[108:111], v194
	ds_read_b128 v[112:115], v194 offset:1024
	ds_read_b128 v[116:119], v194 offset:2048
	ds_read_b128 v[120:123], v194 offset:3072
	ds_read_b128 v[124:127], v195
	ds_read_b128 v[140:143], v195 offset:1024
	ds_read_b128 v[168:171], v195 offset:2048
	ds_read_b128 v[172:175], v195 offset:3072
	s_mov_b32 m0, s64
	v_lshl_add_u64 v[0:1], v[0:1], 0, s[68:69]
	ds_read_b128 v[176:179], v139
	ds_read_b128 v[180:183], v139 offset:1024
	ds_read_b128 v[184:187], v139 offset:2048
	ds_read_b128 v[188:191], v139 offset:3072
	ds_read_b128 v[202:205], v139 offset:4096
	ds_read_b128 v[206:209], v139 offset:5120
	ds_read_b128 v[210:213], v139 offset:6144
	ds_read_b128 v[214:217], v139 offset:7168
	global_load_lds_dwordx4 v[0:1], off
	v_lshl_add_u64 v[0:1], v[2:3], 0, s[68:69]
	s_mov_b32 m0, s2
	s_nop 0
	global_load_lds_dwordx4 v[0:1], off
	s_waitcnt vmcnt(8)
	s_waitcnt lgkmcnt(0)
	s_barrier
	s_setprio 1
	v_mfma_f32_16x16x32_bf16 v[0:3], v[108:111], v[176:179], v[68:71]
	v_mfma_f32_16x16x32_bf16 v[68:71], v[116:119], v[176:179], v[72:75]
	v_mfma_f32_16x16x32_bf16 v[72:75], v[108:111], v[184:187], v[76:79]
	v_mfma_f32_16x16x32_bf16 v[76:79], v[116:119], v[184:187], v[80:83]
	v_mfma_f32_16x16x32_bf16 v[80:83], v[108:111], v[202:205], v[84:87]
	v_mfma_f32_16x16x32_bf16 v[84:87], v[116:119], v[202:205], v[88:91]
	v_mfma_f32_16x16x32_bf16 v[88:91], v[108:111], v[210:213], v[92:95]
	v_mfma_f32_16x16x32_bf16 v[92:95], v[116:119], v[210:213], v[96:99]
	v_mfma_f32_16x16x32_bf16 v[0:3], v[112:115], v[180:183], v[0:3]
	v_mfma_f32_16x16x32_bf16 v[68:71], v[120:123], v[180:183], v[68:71]
	v_mfma_f32_16x16x32_bf16 v[72:75], v[112:115], v[188:191], v[72:75]
	v_mfma_f32_16x16x32_bf16 v[76:79], v[120:123], v[188:191], v[76:79]
	v_mfma_f32_16x16x32_bf16 v[80:83], v[112:115], v[206:209], v[80:83]
	v_mfma_f32_16x16x32_bf16 v[84:87], v[120:123], v[206:209], v[84:87]
	v_mfma_f32_16x16x32_bf16 v[88:91], v[112:115], v[214:217], v[88:91]
	v_mfma_f32_16x16x32_bf16 v[92:95], v[120:123], v[214:217], v[92:95]
	s_setprio 0
	s_setprio 1
	v_mfma_f32_16x16x32_bf16 v[40:43], v[124:127], v[184:187], v[40:43]
	v_mfma_f32_16x16x32_bf16 v[96:99], v[124:127], v[176:179], v[100:103]
	v_mfma_f32_16x16x32_bf16 v[100:103], v[140:143], v[188:191], v[40:43]
	v_mfma_f32_16x16x32_bf16 v[40:43], v[168:171], v[184:187], v[44:47]
	v_mfma_f32_16x16x32_bf16 v[36:39], v[168:171], v[176:179], v[36:39]
	v_mfma_f32_16x16x32_bf16 v[176:179], v[172:175], v[188:191], v[40:43]
	v_mfma_f32_16x16x32_bf16 v[40:43], v[124:127], v[202:205], v[48:51]
	v_mfma_f32_16x16x32_bf16 v[48:51], v[140:143], v[206:209], v[40:43]
	v_mfma_f32_16x16x32_bf16 v[40:43], v[168:171], v[202:205], v[52:55]
	v_mfma_f32_16x16x32_bf16 v[52:55], v[172:175], v[206:209], v[40:43]
	v_mfma_f32_16x16x32_bf16 v[40:43], v[124:127], v[210:213], v[56:59]
	v_mfma_f32_16x16x32_bf16 v[56:59], v[140:143], v[214:217], v[40:43]
	v_mfma_f32_16x16x32_bf16 v[40:43], v[168:171], v[210:213], v[60:63]
	v_mfma_f32_16x16x32_bf16 v[96:99], v[140:143], v[180:183], v[96:99]
	v_mfma_f32_16x16x32_bf16 v[36:39], v[172:175], v[180:183], v[36:39]
	v_mfma_f32_16x16x32_bf16 v[60:63], v[172:175], v[214:217], v[40:43]
	s_setprio 0
	s_barrier
	s_mov_b32 m0, s65
	v_lshl_add_u64 v[250:251], s[56:57], 0, v[192:193]
	s_add_u32 s64, s56, 0x10000
	ds_read_b128 v[40:43], v139 offset:16384
	ds_read_b128 v[44:47], v139 offset:17408
	ds_read_b128 v[180:183], v139 offset:18432
	ds_read_b128 v[184:187], v139 offset:19456
	ds_read_b128 v[188:191], v139 offset:20480
	ds_read_b128 v[202:205], v139 offset:21504
	ds_read_b128 v[206:209], v139 offset:22528
	ds_read_b128 v[210:213], v139 offset:23552
	global_load_lds_dwordx4 v[250:251], off
	v_lshl_add_u64 v[194:195], s[56:57], 0, v[128:129]
	s_mov_b32 m0, s47
	s_addc_u32 s65, s57, 0
	global_load_lds_dwordx4 v[194:195], off
	v_lshl_add_u64 v[214:215], s[64:65], 0, v[192:193]
	s_mov_b32 m0, s49
	v_lshl_add_u64 v[196:197], s[58:59], 0, v[134:135]
	global_load_lds_dwordx4 v[214:215], off
	v_lshl_add_u64 v[214:215], s[64:65], 0, v[128:129]
	s_mov_b32 m0, s63
	v_lshl_add_u64 v[198:199], s[58:59], 0, v[130:131]
	global_load_lds_dwordx4 v[214:215], off
	s_mov_b32 m0, s19
	s_nop 0
	global_load_lds_dwordx4 v[196:197], off
	s_mov_b32 m0, s22
	s_nop 0
	global_load_lds_dwordx4 v[198:199], off
	s_waitcnt vmcnt(8)
	s_waitcnt lgkmcnt(0)
	s_barrier
	s_setprio 1
	v_mfma_f32_16x16x32_bf16 v[144:147], v[108:111], v[40:43], v[144:147]
	v_mfma_f32_16x16x32_bf16 v[152:155], v[108:111], v[180:183], v[152:155]
	v_mfma_f32_16x16x32_bf16 v[160:163], v[108:111], v[188:191], v[160:163]
	v_mfma_f32_16x16x32_bf16 v[4:7], v[108:111], v[206:209], v[4:7]
	v_mfma_f32_16x16x32_bf16 v[8:11], v[116:119], v[206:209], v[8:11]
	v_mfma_f32_16x16x32_bf16 v[144:147], v[112:115], v[44:47], v[144:147]
	v_mfma_f32_16x16x32_bf16 v[148:151], v[116:119], v[40:43], v[148:151]
	v_mfma_f32_16x16x32_bf16 v[152:155], v[112:115], v[184:187], v[152:155]
	v_mfma_f32_16x16x32_bf16 v[156:159], v[116:119], v[180:183], v[156:159]
	v_mfma_f32_16x16x32_bf16 v[160:163], v[112:115], v[202:205], v[160:163]
	v_mfma_f32_16x16x32_bf16 v[164:167], v[116:119], v[188:191], v[164:167]
	v_mfma_f32_16x16x32_bf16 v[4:7], v[112:115], v[210:213], v[4:7]
	v_mfma_f32_16x16x32_bf16 v[112:115], v[120:123], v[210:213], v[8:11]
	v_mfma_f32_16x16x32_bf16 v[148:151], v[120:123], v[44:47], v[148:151]
	v_mfma_f32_16x16x32_bf16 v[156:159], v[120:123], v[184:187], v[156:159]
	v_mfma_f32_16x16x32_bf16 v[164:167], v[120:123], v[202:205], v[164:167]
	s_setprio 0
	s_setprio 1
	v_mfma_f32_16x16x32_bf16 v[8:11], v[124:127], v[40:43], v[12:15]
	v_mfma_f32_16x16x32_bf16 v[116:119], v[140:143], v[44:47], v[8:11]
	v_mfma_f32_16x16x32_bf16 v[8:11], v[168:171], v[40:43], v[16:19]
	v_mfma_f32_16x16x32_bf16 v[16:19], v[172:175], v[44:47], v[8:11]
	v_mfma_f32_16x16x32_bf16 v[8:11], v[124:127], v[180:183], v[28:31]
	v_mfma_f32_16x16x32_bf16 v[214:217], v[140:143], v[184:187], v[8:11]
	v_mfma_f32_16x16x32_bf16 v[8:11], v[168:171], v[180:183], v[32:35]
	v_mfma_f32_16x16x32_bf16 v[180:183], v[172:175], v[184:187], v[8:11]
	v_mfma_f32_16x16x32_bf16 v[8:11], v[124:127], v[188:191], v[64:67]
	v_mfma_f32_16x16x32_bf16 v[184:187], v[140:143], v[202:205], v[8:11]
	v_mfma_f32_16x16x32_bf16 v[8:11], v[168:171], v[188:191], v[104:107]
	v_mfma_f32_16x16x32_bf16 v[188:191], v[172:175], v[202:205], v[8:11]
	v_mfma_f32_16x16x32_bf16 v[8:11], v[124:127], v[206:209], v[20:23]
	v_mfma_f32_16x16x32_bf16 v[20:23], v[140:143], v[210:213], v[8:11]
	v_mfma_f32_16x16x32_bf16 v[8:11], v[168:171], v[206:209], v[24:27]
	v_mfma_f32_16x16x32_bf16 v[140:143], v[172:175], v[210:213], v[8:11]
	s_setprio 0
	s_barrier
	ds_read_b128 v[168:171], v232
	ds_read_b128 v[172:175], v232 offset:1024
	ds_read_b128 v[202:205], v232 offset:2048
	ds_read_b128 v[206:209], v232 offset:3072
	ds_read_b128 v[210:213], v234
	ds_read_b128 v[218:221], v234 offset:1024
	ds_read_b128 v[230:233], v234 offset:2048
	ds_read_b128 v[234:237], v234 offset:3072
	s_mov_b32 m0, s23
	v_lshl_add_u64 v[8:9], s[58:59], 0, v[136:137]
	ds_read_b128 v[24:27], v139 offset:32768
	ds_read_b128 v[28:31], v139 offset:33792
	ds_read_b128 v[32:35], v139 offset:34816
	ds_read_b128 v[64:67], v139 offset:35840
	ds_read_b128 v[238:241], v139 offset:36864
	ds_read_b128 v[242:245], v139 offset:37888
	ds_read_b128 v[246:249], v139 offset:38912
	ds_read_b128 v[226:229], v139 offset:39936
	global_load_lds_dwordx4 v[8:9], off
	v_lshl_add_u64 v[8:9], s[58:59], 0, v[132:133]
	s_mov_b32 m0, s24
	s_nop 0
	global_load_lds_dwordx4 v[8:9], off
	s_waitcnt vmcnt(8)
	s_waitcnt lgkmcnt(0)
	s_barrier
	s_setprio 1
	v_mfma_f32_16x16x32_bf16 v[0:3], v[168:171], v[24:27], v[0:3]
	v_mfma_f32_16x16x32_bf16 v[104:107], v[172:175], v[28:31], v[0:3]
	v_mfma_f32_16x16x32_bf16 v[0:3], v[202:205], v[24:27], v[68:71]
	v_mfma_f32_16x16x32_bf16 v[108:111], v[206:209], v[28:31], v[0:3]
	v_mfma_f32_16x16x32_bf16 v[0:3], v[168:171], v[32:35], v[72:75]
	v_mfma_f32_16x16x32_bf16 v[72:75], v[172:175], v[64:67], v[0:3]
	v_mfma_f32_16x16x32_bf16 v[0:3], v[202:205], v[32:35], v[76:79]
	v_mfma_f32_16x16x32_bf16 v[76:79], v[206:209], v[64:67], v[0:3]
	v_mfma_f32_16x16x32_bf16 v[0:3], v[168:171], v[238:241], v[80:83]
	v_mfma_f32_16x16x32_bf16 v[40:43], v[172:175], v[242:245], v[0:3]
	v_mfma_f32_16x16x32_bf16 v[0:3], v[202:205], v[238:241], v[84:87]
	v_mfma_f32_16x16x32_bf16 v[44:47], v[206:209], v[242:245], v[0:3]
	v_mfma_f32_16x16x32_bf16 v[0:3], v[168:171], v[246:249], v[88:91]
	v_mfma_f32_16x16x32_bf16 v[8:11], v[172:175], v[226:229], v[0:3]
	v_mfma_f32_16x16x32_bf16 v[0:3], v[202:205], v[246:249], v[92:95]
	v_mfma_f32_16x16x32_bf16 v[12:15], v[206:209], v[226:229], v[0:3]
	s_setprio 0
	s_setprio 1
	v_mfma_f32_16x16x32_bf16 v[0:3], v[210:213], v[24:27], v[96:99]
	v_mfma_f32_16x16x32_bf16 v[120:123], v[218:221], v[28:31], v[0:3]
	v_mfma_f32_16x16x32_bf16 v[0:3], v[230:233], v[24:27], v[36:39]
	v_mfma_f32_16x16x32_bf16 v[124:127], v[234:237], v[28:31], v[0:3]
	v_mfma_f32_16x16x32_bf16 v[0:3], v[210:213], v[32:35], v[100:103]
	v_mfma_f32_16x16x32_bf16 v[96:99], v[218:221], v[64:67], v[0:3]
	v_mfma_f32_16x16x32_bf16 v[0:3], v[230:233], v[32:35], v[176:179]
	v_mfma_f32_16x16x32_bf16 v[100:103], v[234:237], v[64:67], v[0:3]
	v_mfma_f32_16x16x32_bf16 v[0:3], v[210:213], v[238:241], v[48:51]
	v_mfma_f32_16x16x32_bf16 v[64:67], v[218:221], v[242:245], v[0:3]
	v_mfma_f32_16x16x32_bf16 v[0:3], v[230:233], v[238:241], v[52:55]
	v_mfma_f32_16x16x32_bf16 v[68:71], v[234:237], v[242:245], v[0:3]
	v_mfma_f32_16x16x32_bf16 v[0:3], v[210:213], v[246:249], v[56:59]
	v_mfma_f32_16x16x32_bf16 v[32:35], v[218:221], v[226:229], v[0:3]
	v_mfma_f32_16x16x32_bf16 v[0:3], v[230:233], v[246:249], v[60:63]
	v_mfma_f32_16x16x32_bf16 v[36:39], v[234:237], v[226:229], v[0:3]
	s_setprio 0
	s_barrier
	s_mov_b32 m0, s61
	s_nop 3
	v_lshl_add_u64 v[0:1], v[250:251], 0, s[26:27]
	s_add_u32 s56, s56, 0x10080
	ds_read_b128 v[48:51], v139 offset:49152
	ds_read_b128 v[52:55], v139 offset:50176
	ds_read_b128 v[84:87], v139 offset:51200
	ds_read_b128 v[176:179], v139 offset:52224
	ds_read_b128 v[226:229], v139 offset:53248
	ds_read_b128 v[238:241], v139 offset:54272
	ds_read_b128 v[242:245], v139 offset:55296
	ds_read_b128 v[246:249], v139 offset:56320
	global_load_lds_dwordx4 v[0:1], off
	v_lshl_add_u64 v[0:1], v[194:195], 0, s[26:27]
	s_mov_b32 m0, s60
	s_addc_u32 s57, s57, 0
	global_load_lds_dwordx4 v[0:1], off
	v_lshl_add_u64 v[0:1], s[56:57], 0, v[192:193]
	s_mov_b32 m0, s54
	s_nop 0
	global_load_lds_dwordx4 v[0:1], off
	v_lshl_add_u64 v[0:1], s[56:57], 0, v[128:129]
	s_mov_b32 m0, s55
	s_nop 0
	global_load_lds_dwordx4 v[0:1], off
	v_lshl_add_u64 v[0:1], v[196:197], 0, s[26:27]
	s_mov_b32 m0, s30
	s_nop 0
	global_load_lds_dwordx4 v[0:1], off
	v_lshl_add_u64 v[0:1], v[198:199], 0, s[26:27]
	s_mov_b32 m0, s31
	s_nop 0
	global_load_lds_dwordx4 v[0:1], off
	s_waitcnt vmcnt(8)
	s_waitcnt lgkmcnt(0)
	s_barrier
	s_setprio 1
	v_mfma_f32_16x16x32_bf16 v[0:3], v[168:171], v[48:51], v[144:147]
	v_mfma_f32_16x16x32_bf16 v[88:91], v[172:175], v[52:55], v[0:3]
	v_mfma_f32_16x16x32_bf16 v[0:3], v[202:205], v[48:51], v[148:151]
	v_mfma_f32_16x16x32_bf16 v[92:95], v[206:209], v[52:55], v[0:3]
	v_mfma_f32_16x16x32_bf16 v[0:3], v[168:171], v[84:87], v[152:155]
	v_mfma_f32_16x16x32_bf16 v[56:59], v[172:175], v[176:179], v[0:3]
	v_mfma_f32_16x16x32_bf16 v[0:3], v[202:205], v[84:87], v[156:159]
	v_mfma_f32_16x16x32_bf16 v[60:63], v[206:209], v[176:179], v[0:3]
	v_mfma_f32_16x16x32_bf16 v[0:3], v[168:171], v[226:229], v[160:163]
	v_mfma_f32_16x16x32_bf16 v[24:27], v[172:175], v[238:241], v[0:3]
	v_mfma_f32_16x16x32_bf16 v[0:3], v[202:205], v[226:229], v[164:167]
	v_mfma_f32_16x16x32_bf16 v[28:31], v[206:209], v[238:241], v[0:3]
	v_mfma_f32_16x16x32_bf16 v[0:3], v[168:171], v[242:245], v[4:7]
	v_mfma_f32_16x16x32_bf16 v[4:7], v[202:205], v[242:245], v[112:115]
	v_mfma_f32_16x16x32_bf16 v[0:3], v[172:175], v[246:249], v[0:3]
	v_mfma_f32_16x16x32_bf16 v[4:7], v[206:209], v[246:249], v[4:7]
	s_setprio 0
	s_setprio 1
	v_mfma_f32_16x16x32_bf16 v[16:19], v[230:233], v[48:51], v[16:19]
	v_mfma_f32_16x16x32_bf16 v[80:83], v[210:213], v[48:51], v[116:119]
	v_mfma_f32_16x16x32_bf16 v[116:119], v[234:237], v[52:55], v[16:19]
	v_mfma_f32_16x16x32_bf16 v[16:19], v[210:213], v[84:87], v[214:217]
	v_mfma_f32_16x16x32_bf16 v[112:115], v[218:221], v[52:55], v[80:83]
	v_mfma_f32_16x16x32_bf16 v[80:83], v[218:221], v[176:179], v[16:19]
	v_mfma_f32_16x16x32_bf16 v[16:19], v[230:233], v[84:87], v[180:183]
	v_mfma_f32_16x16x32_bf16 v[84:87], v[234:237], v[176:179], v[16:19]
	v_mfma_f32_16x16x32_bf16 v[16:19], v[210:213], v[226:229], v[184:187]
	v_mfma_f32_16x16x32_bf16 v[48:51], v[218:221], v[238:241], v[16:19]
	v_mfma_f32_16x16x32_bf16 v[16:19], v[230:233], v[226:229], v[188:191]
	v_mfma_f32_16x16x32_bf16 v[52:55], v[234:237], v[238:241], v[16:19]
	v_mfma_f32_16x16x32_bf16 v[16:19], v[210:213], v[242:245], v[20:23]
	v_mfma_f32_16x16x32_bf16 v[20:23], v[230:233], v[242:245], v[140:143]
	v_mfma_f32_16x16x32_bf16 v[16:19], v[218:221], v[246:249], v[16:19]
	v_mfma_f32_16x16x32_bf16 v[20:23], v[234:237], v[246:249], v[20:23]
	s_setprio 0
	s_barrier
	s_andn2_b64 vcc, exec, s[42:43]
	s_cbranch_vccnz .LBB0_488
	s_barrier

.LBB0_892:
	s_waitcnt vmcnt(8)
	s_add_u32 s2, s54, 0x80
	s_waitcnt lgkmcnt(0)
	s_addc_u32 s12, s55, 0
	s_and_b64 s[4:5], s[4:5], exec
	s_cselect_b32 s5, s41, s12
	s_cselect_b32 s4, s40, s2
	s_cselect_b32 s57, s51, s68
	s_cselect_b32 s56, s66, s67
	s_barrier
	s_setprio 1
	s_waitcnt lgkmcnt(0)
	v_mfma_scale_f32_16x16x128_f8f6f4 v[188:191], v[16:23], v[56:63], v[188:191], v220, v221 op_sel_hi:[0,0,0]
	v_mfma_scale_f32_16x16x128_f8f6f4 v[184:187], v[24:31], v[56:63], v[184:187], v220, v221 op_sel_hi:[0,0,0]
	v_mfma_scale_f32_16x16x128_f8f6f4 v[180:183], v[16:23], v[48:55], v[180:183], v220, v221 op_sel_hi:[0,0,0]
	v_mfma_scale_f32_16x16x128_f8f6f4 v[176:179], v[24:31], v[48:55], v[176:179], v220, v221 op_sel_hi:[0,0,0]
	v_mfma_scale_f32_16x16x128_f8f6f4 v[164:167], v[16:23], v[40:47], v[164:167], v220, v221 op_sel_hi:[0,0,0]
	v_mfma_scale_f32_16x16x128_f8f6f4 v[160:163], v[24:31], v[40:47], v[160:163], v220, v221 op_sel_hi:[0,0,0]
	v_mfma_scale_f32_16x16x128_f8f6f4 v[148:151], v[16:23], v[32:39], v[148:151], v220, v221 op_sel_hi:[0,0,0]
	v_mfma_scale_f32_16x16x128_f8f6f4 v[144:147], v[24:31], v[32:39], v[144:147], v220, v221 op_sel_hi:[0,0,0]
	s_setprio 0
	s_setprio 1
	v_mfma_scale_f32_16x16x128_f8f6f4 v[172:175], v[0:7], v[56:63], v[172:175], v220, v221 op_sel_hi:[0,0,0]
	v_mfma_scale_f32_16x16x128_f8f6f4 v[168:171], v[8:15], v[56:63], v[168:171], v220, v221 op_sel_hi:[0,0,0]
	v_mfma_scale_f32_16x16x128_f8f6f4 v[156:159], v[0:7], v[48:55], v[156:159], v220, v221 op_sel_hi:[0,0,0]
	v_mfma_scale_f32_16x16x128_f8f6f4 v[152:155], v[8:15], v[48:55], v[152:155], v220, v221 op_sel_hi:[0,0,0]
	v_mfma_scale_f32_16x16x128_f8f6f4 v[140:143], v[0:7], v[40:47], v[140:143], v220, v221 op_sel_hi:[0,0,0]
	v_mfma_scale_f32_16x16x128_f8f6f4 v[136:139], v[8:15], v[40:47], v[136:139], v220, v221 op_sel_hi:[0,0,0]
	v_mfma_scale_f32_16x16x128_f8f6f4 v[132:135], v[0:7], v[32:39], v[132:135], v220, v221 op_sel_hi:[0,0,0]
	v_mfma_scale_f32_16x16x128_f8f6f4 v[128:131], v[8:15], v[32:39], v[128:131], v220, v221 op_sel_hi:[0,0,0]
	s_setprio 0
	s_barrier
	s_mov_b32 m0, s22
	v_lshl_add_u64 v[194:195], s[56:57], 0, v[204:205]
	s_add_u32 s12, s56, 0x20000
	ds_read_b128 v[32:35], v235 offset:16384
	ds_read_b128 v[36:39], v235 offset:17408
	ds_read_b128 v[40:43], v235 offset:18432
	ds_read_b128 v[44:47], v235 offset:19456
	ds_read_b128 v[48:51], v235 offset:20480
	ds_read_b128 v[52:55], v235 offset:21504
	ds_read_b128 v[56:59], v235 offset:22528
	ds_read_b128 v[60:63], v235 offset:23552
	global_load_lds_dwordx4 v[194:195], off
	v_lshl_add_u64 v[196:197], s[56:57], 0, v[202:203]
	s_mov_b32 m0, s23
	s_addc_u32 s13, s57, 0
	global_load_lds_dwordx4 v[196:197], off
	v_lshl_add_u64 v[198:199], s[12:13], 0, v[204:205]
	s_mov_b32 m0, s24
	v_mov_b32_e32 v211, v193
	global_load_lds_dwordx4 v[198:199], off
	v_lshl_add_u64 v[198:199], s[12:13], 0, v[202:203]
	s_mov_b32 m0, s25
	v_lshl_add_u64 v[226:227], s[4:5], 0, v[210:211]
	global_load_lds_dwordx4 v[198:199], off
	s_mov_b32 m0, s19
	v_lshl_add_u64 v[198:199], s[4:5], 0, v[192:193]
	global_load_lds_dwordx4 v192, s[4:5]
	s_mov_b32 m0, s28
	s_nop 0
	global_load_lds_dwordx4 v210, s[4:5]
	s_waitcnt vmcnt(8)
	s_waitcnt lgkmcnt(0)
	s_barrier
	s_setprio 1
	v_mfma_scale_f32_16x16x128_f8f6f4 v[124:127], v[16:23], v[32:39], v[124:127], v220, v221 op_sel_hi:[0,0,0]
	v_mfma_scale_f32_16x16x128_f8f6f4 v[120:123], v[24:31], v[32:39], v[120:123], v220, v221 op_sel_hi:[0,0,0]
	v_mfma_scale_f32_16x16x128_f8f6f4 v[116:119], v[16:23], v[40:47], v[116:119], v220, v221 op_sel_hi:[0,0,0]
	v_mfma_scale_f32_16x16x128_f8f6f4 v[112:115], v[24:31], v[40:47], v[112:115], v220, v221 op_sel_hi:[0,0,0]
	v_mfma_scale_f32_16x16x128_f8f6f4 v[100:103], v[16:23], v[48:55], v[100:103], v220, v221 op_sel_hi:[0,0,0]
	v_mfma_scale_f32_16x16x128_f8f6f4 v[96:99], v[24:31], v[48:55], v[96:99], v220, v221 op_sel_hi:[0,0,0]
	v_mfma_scale_f32_16x16x128_f8f6f4 v[84:87], v[16:23], v[56:63], v[84:87], v220, v221 op_sel_hi:[0,0,0]
	v_mfma_scale_f32_16x16x128_f8f6f4 v[80:83], v[24:31], v[56:63], v[80:83], v220, v221 op_sel_hi:[0,0,0]
	s_setprio 0
	s_setprio 1
	v_mfma_scale_f32_16x16x128_f8f6f4 v[108:111], v[0:7], v[32:39], v[108:111], v220, v221 op_sel_hi:[0,0,0]
	v_mfma_scale_f32_16x16x128_f8f6f4 v[104:107], v[8:15], v[32:39], v[104:107], v220, v221 op_sel_hi:[0,0,0]
	v_mfma_scale_f32_16x16x128_f8f6f4 v[92:95], v[0:7], v[40:47], v[92:95], v220, v221 op_sel_hi:[0,0,0]
	v_mfma_scale_f32_16x16x128_f8f6f4 v[88:91], v[8:15], v[40:47], v[88:91], v220, v221 op_sel_hi:[0,0,0]
	v_mfma_scale_f32_16x16x128_f8f6f4 v[76:79], v[0:7], v[48:55], v[76:79], v220, v221 op_sel_hi:[0,0,0]
	v_mfma_scale_f32_16x16x128_f8f6f4 v[72:75], v[8:15], v[48:55], v[72:75], v220, v221 op_sel_hi:[0,0,0]
	v_mfma_scale_f32_16x16x128_f8f6f4 v[68:71], v[0:7], v[56:63], v[68:71], v220, v221 op_sel_hi:[0,0,0]
	v_mfma_scale_f32_16x16x128_f8f6f4 v[64:67], v[8:15], v[56:63], v[64:67], v220, v221 op_sel_hi:[0,0,0]
	s_setprio 0
	s_barrier
	s_add_i32 s2, 0, 0x18000
	s_add_i32 s12, 0, 0x1c000
	v_add_u32_e32 v12, s2, v234
	v_add_u32_e32 v28, s12, v234
	ds_read_b128 v[0:3], v12
	ds_read_b128 v[4:7], v12 offset:1024
	ds_read_b128 v[8:11], v12 offset:2048
	ds_read_b128 v[12:15], v12 offset:3072
	ds_read_b128 v[16:19], v28
	ds_read_b128 v[20:23], v28 offset:1024
	ds_read_b128 v[24:27], v28 offset:2048
	ds_read_b128 v[28:31], v28 offset:3072
	s_mov_b32 m0, s30
	v_lshl_add_u64 v[218:219], s[4:5], 0, v[218:219]
	ds_read_b128 v[32:35], v235 offset:32768
	ds_read_b128 v[36:39], v235 offset:33792
	ds_read_b128 v[40:43], v235 offset:34816
	ds_read_b128 v[44:47], v235 offset:35840
	ds_read_b128 v[48:51], v235 offset:36864
	ds_read_b128 v[52:55], v235 offset:37888
	ds_read_b128 v[56:59], v235 offset:38912
	ds_read_b128 v[60:63], v235 offset:39936
	global_load_lds_dwordx4 v[218:219], off
	v_lshl_add_u64 v[216:217], s[4:5], 0, v[216:217]
	s_mov_b32 m0, s31
	s_nop 0
	global_load_lds_dwordx4 v[216:217], off
	s_waitcnt vmcnt(8)
	s_waitcnt lgkmcnt(0)
	s_barrier
	s_setprio 1
	v_mfma_scale_f32_16x16x128_f8f6f4 v[188:191], v[0:7], v[32:39], v[188:191], v220, v221 op_sel_hi:[0,0,0]
	v_mfma_scale_f32_16x16x128_f8f6f4 v[184:187], v[8:15], v[32:39], v[184:187], v220, v221 op_sel_hi:[0,0,0]
	v_mfma_scale_f32_16x16x128_f8f6f4 v[180:183], v[0:7], v[40:47], v[180:183], v220, v221 op_sel_hi:[0,0,0]
	v_mfma_scale_f32_16x16x128_f8f6f4 v[176:179], v[8:15], v[40:47], v[176:179], v220, v221 op_sel_hi:[0,0,0]
	v_mfma_scale_f32_16x16x128_f8f6f4 v[164:167], v[0:7], v[48:55], v[164:167], v220, v221 op_sel_hi:[0,0,0]
	v_mfma_scale_f32_16x16x128_f8f6f4 v[160:163], v[8:15], v[48:55], v[160:163], v220, v221 op_sel_hi:[0,0,0]
	v_mfma_scale_f32_16x16x128_f8f6f4 v[148:151], v[0:7], v[56:63], v[148:151], v220, v221 op_sel_hi:[0,0,0]
	v_mfma_scale_f32_16x16x128_f8f6f4 v[144:147], v[8:15], v[56:63], v[144:147], v220, v221 op_sel_hi:[0,0,0]
	s_setprio 0
	s_setprio 1
	v_mfma_scale_f32_16x16x128_f8f6f4 v[172:175], v[16:23], v[32:39], v[172:175], v220, v221 op_sel_hi:[0,0,0]
	v_mfma_scale_f32_16x16x128_f8f6f4 v[168:171], v[24:31], v[32:39], v[168:171], v220, v221 op_sel_hi:[0,0,0]
	v_mfma_scale_f32_16x16x128_f8f6f4 v[156:159], v[16:23], v[40:47], v[156:159], v220, v221 op_sel_hi:[0,0,0]
	v_mfma_scale_f32_16x16x128_f8f6f4 v[152:155], v[24:31], v[40:47], v[152:155], v220, v221 op_sel_hi:[0,0,0]
	v_mfma_scale_f32_16x16x128_f8f6f4 v[140:143], v[16:23], v[48:55], v[140:143], v220, v221 op_sel_hi:[0,0,0]
	v_mfma_scale_f32_16x16x128_f8f6f4 v[136:139], v[24:31], v[48:55], v[136:139], v220, v221 op_sel_hi:[0,0,0]
	v_mfma_scale_f32_16x16x128_f8f6f4 v[132:135], v[16:23], v[56:63], v[132:135], v220, v221 op_sel_hi:[0,0,0]
	v_mfma_scale_f32_16x16x128_f8f6f4 v[128:131], v[24:31], v[56:63], v[128:131], v220, v221 op_sel_hi:[0,0,0]
	s_setprio 0
	s_barrier
	s_add_i32 s2, s2, s9
	v_lshl_add_u64 v[194:195], v[194:195], 0, s[26:27]
	s_mov_b32 m0, s2
	ds_read_b128 v[32:35], v235 offset:49152
	ds_read_b128 v[36:39], v235 offset:50176
	ds_read_b128 v[40:43], v235 offset:51200
	ds_read_b128 v[44:47], v235 offset:52224
	ds_read_b128 v[48:51], v235 offset:53248
	ds_read_b128 v[52:55], v235 offset:54272
	ds_read_b128 v[56:59], v235 offset:55296
	ds_read_b128 v[60:63], v235 offset:56320
	global_load_lds_dwordx4 v[194:195], off
	s_add_i32 m0, s2, 0x2000
	s_add_u32 s4, s56, 0x20080
	v_lshl_add_u64 v[194:195], v[196:197], 0, s[26:27]
	s_addc_u32 s5, s57, 0
	s_add_i32 s2, s12, s9
	global_load_lds_dwordx4 v[194:195], off
	v_lshl_add_u64 v[194:195], s[4:5], 0, v[204:205]
	s_mov_b32 m0, s2
	s_nop 0
	global_load_lds_dwordx4 v[194:195], off
	v_lshl_add_u64 v[194:195], s[4:5], 0, v[202:203]
	s_add_i32 m0, s2, 0x2000
	s_nop 0
	global_load_lds_dwordx4 v[194:195], off
	v_lshl_add_u64 v[194:195], v[198:199], 0, s[26:27]
	s_mov_b32 m0, s60
	s_nop 0
	global_load_lds_dwordx4 v[194:195], off
	v_lshl_add_u64 v[194:195], v[226:227], 0, s[26:27]
	s_mov_b32 m0, s61
	s_nop 0
	global_load_lds_dwordx4 v[194:195], off
	s_waitcnt vmcnt(8)
	s_waitcnt lgkmcnt(0)
	s_barrier
	s_setprio 1
	v_mfma_scale_f32_16x16x128_f8f6f4 v[124:127], v[0:7], v[32:39], v[124:127], v220, v221 op_sel_hi:[0,0,0]
	v_mfma_scale_f32_16x16x128_f8f6f4 v[120:123], v[8:15], v[32:39], v[120:123], v220, v221 op_sel_hi:[0,0,0]
	v_mfma_scale_f32_16x16x128_f8f6f4 v[116:119], v[0:7], v[40:47], v[116:119], v220, v221 op_sel_hi:[0,0,0]
	v_mfma_scale_f32_16x16x128_f8f6f4 v[112:115], v[8:15], v[40:47], v[112:115], v220, v221 op_sel_hi:[0,0,0]
	v_mfma_scale_f32_16x16x128_f8f6f4 v[100:103], v[0:7], v[48:55], v[100:103], v220, v221 op_sel_hi:[0,0,0]
	v_mfma_scale_f32_16x16x128_f8f6f4 v[96:99], v[8:15], v[48:55], v[96:99], v220, v221 op_sel_hi:[0,0,0]
	v_mfma_scale_f32_16x16x128_f8f6f4 v[84:87], v[0:7], v[56:63], v[84:87], v220, v221 op_sel_hi:[0,0,0]
	v_mfma_scale_f32_16x16x128_f8f6f4 v[80:83], v[8:15], v[56:63], v[80:83], v220, v221 op_sel_hi:[0,0,0]
	s_setprio 0
	s_setprio 1
	v_mfma_scale_f32_16x16x128_f8f6f4 v[108:111], v[16:23], v[32:39], v[108:111], v220, v221 op_sel_hi:[0,0,0]
	v_mfma_scale_f32_16x16x128_f8f6f4 v[104:107], v[24:31], v[32:39], v[104:107], v220, v221 op_sel_hi:[0,0,0]
	v_mfma_scale_f32_16x16x128_f8f6f4 v[92:95], v[16:23], v[40:47], v[92:95], v220, v221 op_sel_hi:[0,0,0]
	v_mfma_scale_f32_16x16x128_f8f6f4 v[88:91], v[24:31], v[40:47], v[88:91], v220, v221 op_sel_hi:[0,0,0]
	v_mfma_scale_f32_16x16x128_f8f6f4 v[76:79], v[16:23], v[48:55], v[76:79], v220, v221 op_sel_hi:[0,0,0]
	v_mfma_scale_f32_16x16x128_f8f6f4 v[72:75], v[24:31], v[48:55], v[72:75], v220, v221 op_sel_hi:[0,0,0]
	v_mfma_scale_f32_16x16x128_f8f6f4 v[68:71], v[16:23], v[56:63], v[68:71], v220, v221 op_sel_hi:[0,0,0]
	v_mfma_scale_f32_16x16x128_f8f6f4 v[64:67], v[24:31], v[56:63], v[64:67], v220, v221 op_sel_hi:[0,0,0]
	s_setprio 0
	s_barrier
	s_add_i32 s69, s69, 2
	s_add_u32 s54, s54, 0x100
	s_addc_u32 s55, s55, 0
	s_add_u32 s67, s67, 0x100
	s_addc_u32 s68, s68, 0
	s_cmp_gt_u32 s69, 5
	s_cbranch_scc1 .LBB0_895

.LBB0_1187:
	s_waitcnt vmcnt(8)
	s_add_u32 s2, s68, 0x80
	s_waitcnt lgkmcnt(0)
	s_addc_u32 s12, s69, 0
	s_and_b64 s[4:5], s[4:5], exec
	s_cselect_b32 s5, s43, s12
	s_cselect_b32 s4, s42, s2
	s_cselect_b32 s71, s7, s87
	s_cselect_b32 s70, s63, s86
	s_barrier
	s_setprio 1
	s_waitcnt lgkmcnt(0)
	v_mfma_scale_f32_16x16x128_f8f6f4 v[188:191], v[16:23], v[56:63], v[188:191], v213, v216 op_sel_hi:[0,0,0]
	v_mfma_scale_f32_16x16x128_f8f6f4 v[180:183], v[24:31], v[56:63], v[180:183], v213, v216 op_sel_hi:[0,0,0]
	v_mfma_scale_f32_16x16x128_f8f6f4 v[172:175], v[16:23], v[48:55], v[172:175], v213, v216 op_sel_hi:[0,0,0]
	v_mfma_scale_f32_16x16x128_f8f6f4 v[164:167], v[24:31], v[48:55], v[164:167], v213, v216 op_sel_hi:[0,0,0]
	v_mfma_scale_f32_16x16x128_f8f6f4 v[156:159], v[16:23], v[40:47], v[156:159], v213, v216 op_sel_hi:[0,0,0]
	v_mfma_scale_f32_16x16x128_f8f6f4 v[148:151], v[24:31], v[40:47], v[148:151], v213, v216 op_sel_hi:[0,0,0]
	v_mfma_scale_f32_16x16x128_f8f6f4 v[140:143], v[16:23], v[32:39], v[140:143], v213, v216 op_sel_hi:[0,0,0]
	v_mfma_scale_f32_16x16x128_f8f6f4 v[132:135], v[24:31], v[32:39], v[132:135], v213, v216 op_sel_hi:[0,0,0]
	s_setprio 0
	s_setprio 1
	v_mfma_scale_f32_16x16x128_f8f6f4 v[184:187], v[0:7], v[56:63], v[184:187], v213, v216 op_sel_hi:[0,0,0]
	v_mfma_scale_f32_16x16x128_f8f6f4 v[176:179], v[8:15], v[56:63], v[176:179], v213, v216 op_sel_hi:[0,0,0]
	v_mfma_scale_f32_16x16x128_f8f6f4 v[168:171], v[0:7], v[48:55], v[168:171], v213, v216 op_sel_hi:[0,0,0]
	v_mfma_scale_f32_16x16x128_f8f6f4 v[160:163], v[8:15], v[48:55], v[160:163], v213, v216 op_sel_hi:[0,0,0]
	v_mfma_scale_f32_16x16x128_f8f6f4 v[152:155], v[0:7], v[40:47], v[152:155], v213, v216 op_sel_hi:[0,0,0]
	v_mfma_scale_f32_16x16x128_f8f6f4 v[144:147], v[8:15], v[40:47], v[144:147], v213, v216 op_sel_hi:[0,0,0]
	v_mfma_scale_f32_16x16x128_f8f6f4 v[136:139], v[0:7], v[32:39], v[136:139], v213, v216 op_sel_hi:[0,0,0]
	v_mfma_scale_f32_16x16x128_f8f6f4 v[128:131], v[8:15], v[32:39], v[128:131], v213, v216 op_sel_hi:[0,0,0]
	s_setprio 0
	s_barrier
	s_mov_b32 m0, s75
	v_lshl_add_u64 v[194:195], s[70:71], 0, v[204:205]
	s_add_u32 s12, s70, 0x20000
	ds_read_b128 v[32:35], v233 offset:16384
	ds_read_b128 v[36:39], v233 offset:17408
	ds_read_b128 v[40:43], v233 offset:18432
	ds_read_b128 v[44:47], v233 offset:19456
	ds_read_b128 v[48:51], v233 offset:20480
	ds_read_b128 v[52:55], v233 offset:21504
	ds_read_b128 v[56:59], v233 offset:22528
	ds_read_b128 v[60:63], v233 offset:23552
	global_load_lds_dwordx4 v[194:195], off
	v_lshl_add_u64 v[196:197], s[70:71], 0, v[202:203]
	s_mov_b32 m0, s76
	s_addc_u32 s13, s71, 0
	global_load_lds_dwordx4 v[196:197], off
	v_lshl_add_u64 v[198:199], s[12:13], 0, v[204:205]
	s_mov_b32 m0, s77
	v_mov_b32_e32 v209, v193
	global_load_lds_dwordx4 v[198:199], off
	v_lshl_add_u64 v[198:199], s[12:13], 0, v[202:203]
	s_mov_b32 m0, s80
	v_lshl_add_u64 v[226:227], s[4:5], 0, v[208:209]
	global_load_lds_dwordx4 v[198:199], off
	s_mov_b32 m0, s74
	v_lshl_add_u64 v[198:199], s[4:5], 0, v[192:193]
	global_load_lds_dwordx4 v192, s[4:5]
	s_mov_b32 m0, s81
	s_nop 0
	global_load_lds_dwordx4 v208, s[4:5]
	s_waitcnt vmcnt(8)
	s_waitcnt lgkmcnt(0)
	s_barrier
	s_setprio 1
	v_mfma_scale_f32_16x16x128_f8f6f4 v[124:127], v[16:23], v[32:39], v[124:127], v213, v216 op_sel_hi:[0,0,0]
	v_mfma_scale_f32_16x16x128_f8f6f4 v[116:119], v[24:31], v[32:39], v[116:119], v213, v216 op_sel_hi:[0,0,0]
	v_mfma_scale_f32_16x16x128_f8f6f4 v[108:111], v[16:23], v[40:47], v[108:111], v213, v216 op_sel_hi:[0,0,0]
	v_mfma_scale_f32_16x16x128_f8f6f4 v[100:103], v[24:31], v[40:47], v[100:103], v213, v216 op_sel_hi:[0,0,0]
	v_mfma_scale_f32_16x16x128_f8f6f4 v[92:95], v[16:23], v[48:55], v[92:95], v213, v216 op_sel_hi:[0,0,0]
	v_mfma_scale_f32_16x16x128_f8f6f4 v[84:87], v[24:31], v[48:55], v[84:87], v213, v216 op_sel_hi:[0,0,0]
	v_mfma_scale_f32_16x16x128_f8f6f4 v[76:79], v[16:23], v[56:63], v[76:79], v213, v216 op_sel_hi:[0,0,0]
	v_mfma_scale_f32_16x16x128_f8f6f4 v[68:71], v[24:31], v[56:63], v[68:71], v213, v216 op_sel_hi:[0,0,0]
	s_setprio 0
	s_setprio 1
	v_mfma_scale_f32_16x16x128_f8f6f4 v[120:123], v[0:7], v[32:39], v[120:123], v213, v216 op_sel_hi:[0,0,0]
	v_mfma_scale_f32_16x16x128_f8f6f4 v[112:115], v[8:15], v[32:39], v[112:115], v213, v216 op_sel_hi:[0,0,0]
	v_mfma_scale_f32_16x16x128_f8f6f4 v[104:107], v[0:7], v[40:47], v[104:107], v213, v216 op_sel_hi:[0,0,0]
	v_mfma_scale_f32_16x16x128_f8f6f4 v[96:99], v[8:15], v[40:47], v[96:99], v213, v216 op_sel_hi:[0,0,0]
	v_mfma_scale_f32_16x16x128_f8f6f4 v[88:91], v[0:7], v[48:55], v[88:91], v213, v216 op_sel_hi:[0,0,0]
	v_mfma_scale_f32_16x16x128_f8f6f4 v[80:83], v[8:15], v[48:55], v[80:83], v213, v216 op_sel_hi:[0,0,0]
	v_mfma_scale_f32_16x16x128_f8f6f4 v[72:75], v[0:7], v[56:63], v[72:75], v213, v216 op_sel_hi:[0,0,0]
	v_mfma_scale_f32_16x16x128_f8f6f4 v[64:67], v[8:15], v[56:63], v[64:67], v213, v216 op_sel_hi:[0,0,0]
	s_setprio 0
	s_barrier
	s_add_i32 s2, 0, 0x18000
	s_add_i32 s12, 0, 0x1c000
	v_add_u32_e32 v12, s2, v221
	v_add_u32_e32 v28, s12, v221
	ds_read_b128 v[0:3], v12
	ds_read_b128 v[4:7], v12 offset:1024
	ds_read_b128 v[8:11], v12 offset:2048
	ds_read_b128 v[12:15], v12 offset:3072
	ds_read_b128 v[16:19], v28
	ds_read_b128 v[20:23], v28 offset:1024
	ds_read_b128 v[24:27], v28 offset:2048
	ds_read_b128 v[28:31], v28 offset:3072
	s_mov_b32 m0, s88
	v_lshl_add_u64 v[214:215], s[4:5], 0, v[214:215]
	ds_read_b128 v[32:35], v233 offset:32768
	ds_read_b128 v[36:39], v233 offset:33792
	ds_read_b128 v[40:43], v233 offset:34816
	ds_read_b128 v[44:47], v233 offset:35840
	ds_read_b128 v[48:51], v233 offset:36864
	ds_read_b128 v[52:55], v233 offset:37888
	ds_read_b128 v[56:59], v233 offset:38912
	ds_read_b128 v[60:63], v233 offset:39936
	global_load_lds_dwordx4 v[214:215], off
	v_lshl_add_u64 v[214:215], s[4:5], 0, v[210:211]
	s_mov_b32 m0, s89
	s_nop 0
	global_load_lds_dwordx4 v[214:215], off
	s_waitcnt vmcnt(8)
	s_waitcnt lgkmcnt(0)
	s_barrier
	s_setprio 1
	v_mfma_scale_f32_16x16x128_f8f6f4 v[188:191], v[0:7], v[32:39], v[188:191], v213, v216 op_sel_hi:[0,0,0]
	v_mfma_scale_f32_16x16x128_f8f6f4 v[180:183], v[8:15], v[32:39], v[180:183], v213, v216 op_sel_hi:[0,0,0]
	v_mfma_scale_f32_16x16x128_f8f6f4 v[172:175], v[0:7], v[40:47], v[172:175], v213, v216 op_sel_hi:[0,0,0]
	v_mfma_scale_f32_16x16x128_f8f6f4 v[164:167], v[8:15], v[40:47], v[164:167], v213, v216 op_sel_hi:[0,0,0]
	v_mfma_scale_f32_16x16x128_f8f6f4 v[156:159], v[0:7], v[48:55], v[156:159], v213, v216 op_sel_hi:[0,0,0]
	v_mfma_scale_f32_16x16x128_f8f6f4 v[148:151], v[8:15], v[48:55], v[148:151], v213, v216 op_sel_hi:[0,0,0]
	v_mfma_scale_f32_16x16x128_f8f6f4 v[140:143], v[0:7], v[56:63], v[140:143], v213, v216 op_sel_hi:[0,0,0]
	v_mfma_scale_f32_16x16x128_f8f6f4 v[132:135], v[8:15], v[56:63], v[132:135], v213, v216 op_sel_hi:[0,0,0]
	s_setprio 0
	s_setprio 1
	v_mfma_scale_f32_16x16x128_f8f6f4 v[184:187], v[16:23], v[32:39], v[184:187], v213, v216 op_sel_hi:[0,0,0]
	v_mfma_scale_f32_16x16x128_f8f6f4 v[176:179], v[24:31], v[32:39], v[176:179], v213, v216 op_sel_hi:[0,0,0]
	v_mfma_scale_f32_16x16x128_f8f6f4 v[168:171], v[16:23], v[40:47], v[168:171], v213, v216 op_sel_hi:[0,0,0]
	v_mfma_scale_f32_16x16x128_f8f6f4 v[160:163], v[24:31], v[40:47], v[160:163], v213, v216 op_sel_hi:[0,0,0]
	v_mfma_scale_f32_16x16x128_f8f6f4 v[152:155], v[16:23], v[48:55], v[152:155], v213, v216 op_sel_hi:[0,0,0]
	v_mfma_scale_f32_16x16x128_f8f6f4 v[144:147], v[24:31], v[48:55], v[144:147], v213, v216 op_sel_hi:[0,0,0]
	v_mfma_scale_f32_16x16x128_f8f6f4 v[136:139], v[16:23], v[56:63], v[136:139], v213, v216 op_sel_hi:[0,0,0]
	v_mfma_scale_f32_16x16x128_f8f6f4 v[128:131], v[24:31], v[56:63], v[128:131], v213, v216 op_sel_hi:[0,0,0]
	s_setprio 0
	s_barrier
	s_add_i32 s2, s2, s31
	v_lshl_add_u64 v[194:195], v[194:195], 0, s[26:27]
	s_mov_b32 m0, s2
	ds_read_b128 v[32:35], v233 offset:49152
	ds_read_b128 v[36:39], v233 offset:50176
	ds_read_b128 v[40:43], v233 offset:51200
	ds_read_b128 v[44:47], v233 offset:52224
	ds_read_b128 v[48:51], v233 offset:53248
	ds_read_b128 v[52:55], v233 offset:54272
	ds_read_b128 v[56:59], v233 offset:55296
	ds_read_b128 v[60:63], v233 offset:56320
	global_load_lds_dwordx4 v[194:195], off
	s_add_i32 m0, s2, 0x2000
	s_add_u32 s4, s70, 0x20080
	v_lshl_add_u64 v[194:195], v[196:197], 0, s[26:27]
	s_addc_u32 s5, s71, 0
	s_add_i32 s2, s12, s31
	global_load_lds_dwordx4 v[194:195], off
	v_lshl_add_u64 v[194:195], s[4:5], 0, v[204:205]
	s_mov_b32 m0, s2
	s_nop 0
	global_load_lds_dwordx4 v[194:195], off
	v_lshl_add_u64 v[194:195], s[4:5], 0, v[202:203]
	s_add_i32 m0, s2, 0x2000
	s_nop 0
	global_load_lds_dwordx4 v[194:195], off
	v_lshl_add_u64 v[194:195], v[198:199], 0, s[26:27]
	s_mov_b32 m0, s91
	s_nop 0
	global_load_lds_dwordx4 v[194:195], off
	v_lshl_add_u64 v[194:195], v[226:227], 0, s[26:27]
	s_mov_b32 m0, s92
	s_nop 0
	global_load_lds_dwordx4 v[194:195], off
	s_waitcnt vmcnt(8)
	s_waitcnt lgkmcnt(0)
	s_barrier
	s_setprio 1
	v_mfma_scale_f32_16x16x128_f8f6f4 v[124:127], v[0:7], v[32:39], v[124:127], v213, v216 op_sel_hi:[0,0,0]
	v_mfma_scale_f32_16x16x128_f8f6f4 v[116:119], v[8:15], v[32:39], v[116:119], v213, v216 op_sel_hi:[0,0,0]
	v_mfma_scale_f32_16x16x128_f8f6f4 v[108:111], v[0:7], v[40:47], v[108:111], v213, v216 op_sel_hi:[0,0,0]
	v_mfma_scale_f32_16x16x128_f8f6f4 v[100:103], v[8:15], v[40:47], v[100:103], v213, v216 op_sel_hi:[0,0,0]
	v_mfma_scale_f32_16x16x128_f8f6f4 v[92:95], v[0:7], v[48:55], v[92:95], v213, v216 op_sel_hi:[0,0,0]
	v_mfma_scale_f32_16x16x128_f8f6f4 v[84:87], v[8:15], v[48:55], v[84:87], v213, v216 op_sel_hi:[0,0,0]
	v_mfma_scale_f32_16x16x128_f8f6f4 v[76:79], v[0:7], v[56:63], v[76:79], v213, v216 op_sel_hi:[0,0,0]
	v_mfma_scale_f32_16x16x128_f8f6f4 v[68:71], v[8:15], v[56:63], v[68:71], v213, v216 op_sel_hi:[0,0,0]
	s_setprio 0
	s_setprio 1
	v_mfma_scale_f32_16x16x128_f8f6f4 v[120:123], v[16:23], v[32:39], v[120:123], v213, v216 op_sel_hi:[0,0,0]
	v_mfma_scale_f32_16x16x128_f8f6f4 v[112:115], v[24:31], v[32:39], v[112:115], v213, v216 op_sel_hi:[0,0,0]
	v_mfma_scale_f32_16x16x128_f8f6f4 v[104:107], v[16:23], v[40:47], v[104:107], v213, v216 op_sel_hi:[0,0,0]
	v_mfma_scale_f32_16x16x128_f8f6f4 v[96:99], v[24:31], v[40:47], v[96:99], v213, v216 op_sel_hi:[0,0,0]
	v_mfma_scale_f32_16x16x128_f8f6f4 v[88:91], v[16:23], v[48:55], v[88:91], v213, v216 op_sel_hi:[0,0,0]
	v_mfma_scale_f32_16x16x128_f8f6f4 v[80:83], v[24:31], v[48:55], v[80:83], v213, v216 op_sel_hi:[0,0,0]
	v_mfma_scale_f32_16x16x128_f8f6f4 v[72:75], v[16:23], v[56:63], v[72:75], v213, v216 op_sel_hi:[0,0,0]
	v_mfma_scale_f32_16x16x128_f8f6f4 v[64:67], v[24:31], v[56:63], v[64:67], v213, v216 op_sel_hi:[0,0,0]
	s_setprio 0
	s_barrier
	s_add_i32 s40, s40, 2
	s_add_u32 s68, s68, 0x100
	s_addc_u32 s69, s69, 0
	s_add_u32 s86, s86, 0x100
	s_addc_u32 s87, s87, 0
	s_cmp_gt_u32 s40, 5
	s_cbranch_scc1 .LBB0_1190

.LBB0_1322:
	s_waitcnt vmcnt(8)
	s_add_u32 s2, s64, 0x80
	s_waitcnt lgkmcnt(0)
	s_addc_u32 s12, s65, 0
	s_and_b64 s[4:5], s[4:5], exec
	s_cselect_b32 s5, s43, s12
	s_cselect_b32 s4, s42, s2
	s_cselect_b32 s67, s7, s83
	s_cselect_b32 s66, s59, s61
	s_barrier
	s_setprio 1
	s_waitcnt lgkmcnt(0)
	v_mfma_scale_f32_16x16x128_f8f6f4 v[188:191], v[16:23], v[56:63], v[188:191], v220, v221 op_sel_hi:[0,0,0]
	v_mfma_scale_f32_16x16x128_f8f6f4 v[184:187], v[24:31], v[56:63], v[184:187], v220, v221 op_sel_hi:[0,0,0]
	v_mfma_scale_f32_16x16x128_f8f6f4 v[172:175], v[16:23], v[48:55], v[172:175], v220, v221 op_sel_hi:[0,0,0]
	v_mfma_scale_f32_16x16x128_f8f6f4 v[168:171], v[24:31], v[48:55], v[168:171], v220, v221 op_sel_hi:[0,0,0]
	v_mfma_scale_f32_16x16x128_f8f6f4 v[156:159], v[16:23], v[40:47], v[156:159], v220, v221 op_sel_hi:[0,0,0]
	v_mfma_scale_f32_16x16x128_f8f6f4 v[152:155], v[24:31], v[40:47], v[152:155], v220, v221 op_sel_hi:[0,0,0]
	v_mfma_scale_f32_16x16x128_f8f6f4 v[140:143], v[16:23], v[32:39], v[140:143], v220, v221 op_sel_hi:[0,0,0]
	v_mfma_scale_f32_16x16x128_f8f6f4 v[136:139], v[24:31], v[32:39], v[136:139], v220, v221 op_sel_hi:[0,0,0]
	s_setprio 0
	s_setprio 1
	v_mfma_scale_f32_16x16x128_f8f6f4 v[180:183], v[0:7], v[56:63], v[180:183], v220, v221 op_sel_hi:[0,0,0]
	v_mfma_scale_f32_16x16x128_f8f6f4 v[176:179], v[8:15], v[56:63], v[176:179], v220, v221 op_sel_hi:[0,0,0]
	v_mfma_scale_f32_16x16x128_f8f6f4 v[164:167], v[0:7], v[48:55], v[164:167], v220, v221 op_sel_hi:[0,0,0]
	v_mfma_scale_f32_16x16x128_f8f6f4 v[160:163], v[8:15], v[48:55], v[160:163], v220, v221 op_sel_hi:[0,0,0]
	v_mfma_scale_f32_16x16x128_f8f6f4 v[148:151], v[0:7], v[40:47], v[148:151], v220, v221 op_sel_hi:[0,0,0]
	v_mfma_scale_f32_16x16x128_f8f6f4 v[144:147], v[8:15], v[40:47], v[144:147], v220, v221 op_sel_hi:[0,0,0]
	v_mfma_scale_f32_16x16x128_f8f6f4 v[132:135], v[0:7], v[32:39], v[132:135], v220, v221 op_sel_hi:[0,0,0]
	v_mfma_scale_f32_16x16x128_f8f6f4 v[128:131], v[8:15], v[32:39], v[128:131], v220, v221 op_sel_hi:[0,0,0]
	s_setprio 0
	s_barrier
	s_mov_b32 m0, s72
	v_lshl_add_u64 v[194:195], s[66:67], 0, v[202:203]
	s_add_u32 s12, s66, 0x20000
	ds_read_b128 v[32:35], v237 offset:16384
	ds_read_b128 v[36:39], v237 offset:17408
	ds_read_b128 v[40:43], v237 offset:18432
	ds_read_b128 v[44:47], v237 offset:19456
	ds_read_b128 v[48:51], v237 offset:20480
	ds_read_b128 v[52:55], v237 offset:21504
	ds_read_b128 v[56:59], v237 offset:22528
	ds_read_b128 v[60:63], v237 offset:23552
	global_load_lds_dwordx4 v[194:195], off
	v_lshl_add_u64 v[196:197], s[66:67], 0, v[204:205]
	s_mov_b32 m0, s73
	s_addc_u32 s13, s67, 0
	global_load_lds_dwordx4 v[196:197], off
	v_lshl_add_u64 v[198:199], s[12:13], 0, v[202:203]
	s_mov_b32 m0, s74
	v_mov_b32_e32 v211, v193
	global_load_lds_dwordx4 v[198:199], off
	v_lshl_add_u64 v[198:199], s[12:13], 0, v[204:205]
	s_mov_b32 m0, s75
	v_lshl_add_u64 v[226:227], s[4:5], 0, v[210:211]
	global_load_lds_dwordx4 v[198:199], off
	s_mov_b32 m0, s71
	v_lshl_add_u64 v[198:199], s[4:5], 0, v[192:193]
	global_load_lds_dwordx4 v192, s[4:5]
	s_mov_b32 m0, s76
	s_nop 0
	global_load_lds_dwordx4 v210, s[4:5]
	s_waitcnt vmcnt(8)
	s_waitcnt lgkmcnt(0)
	s_barrier
	s_setprio 1
	v_mfma_scale_f32_16x16x128_f8f6f4 v[124:127], v[16:23], v[32:39], v[124:127], v220, v221 op_sel_hi:[0,0,0]
	v_mfma_scale_f32_16x16x128_f8f6f4 v[120:123], v[24:31], v[32:39], v[120:123], v220, v221 op_sel_hi:[0,0,0]
	v_mfma_scale_f32_16x16x128_f8f6f4 v[108:111], v[16:23], v[40:47], v[108:111], v220, v221 op_sel_hi:[0,0,0]
	v_mfma_scale_f32_16x16x128_f8f6f4 v[104:107], v[24:31], v[40:47], v[104:107], v220, v221 op_sel_hi:[0,0,0]
	v_mfma_scale_f32_16x16x128_f8f6f4 v[92:95], v[16:23], v[48:55], v[92:95], v220, v221 op_sel_hi:[0,0,0]
	v_mfma_scale_f32_16x16x128_f8f6f4 v[88:91], v[24:31], v[48:55], v[88:91], v220, v221 op_sel_hi:[0,0,0]
	v_mfma_scale_f32_16x16x128_f8f6f4 v[72:75], v[16:23], v[56:63], v[72:75], v220, v221 op_sel_hi:[0,0,0]
	v_mfma_scale_f32_16x16x128_f8f6f4 v[76:79], v[24:31], v[56:63], v[76:79], v220, v221 op_sel_hi:[0,0,0]
	s_setprio 0
	s_setprio 1
	v_mfma_scale_f32_16x16x128_f8f6f4 v[116:119], v[0:7], v[32:39], v[116:119], v220, v221 op_sel_hi:[0,0,0]
	v_mfma_scale_f32_16x16x128_f8f6f4 v[112:115], v[8:15], v[32:39], v[112:115], v220, v221 op_sel_hi:[0,0,0]
	v_mfma_scale_f32_16x16x128_f8f6f4 v[100:103], v[0:7], v[40:47], v[100:103], v220, v221 op_sel_hi:[0,0,0]
	v_mfma_scale_f32_16x16x128_f8f6f4 v[96:99], v[8:15], v[40:47], v[96:99], v220, v221 op_sel_hi:[0,0,0]
	v_mfma_scale_f32_16x16x128_f8f6f4 v[84:87], v[0:7], v[48:55], v[84:87], v220, v221 op_sel_hi:[0,0,0]
	v_mfma_scale_f32_16x16x128_f8f6f4 v[80:83], v[8:15], v[48:55], v[80:83], v220, v221 op_sel_hi:[0,0,0]
	v_mfma_scale_f32_16x16x128_f8f6f4 v[64:67], v[0:7], v[56:63], v[64:67], v220, v221 op_sel_hi:[0,0,0]
	v_mfma_scale_f32_16x16x128_f8f6f4 v[68:71], v[8:15], v[56:63], v[68:71], v220, v221 op_sel_hi:[0,0,0]
	s_setprio 0
	s_barrier
	s_add_i32 s2, 0, 0x18000
	s_add_i32 s12, 0, 0x1c000
	v_add_u32_e32 v12, s2, v234
	v_add_u32_e32 v28, s12, v234
	ds_read_b128 v[0:3], v12
	ds_read_b128 v[4:7], v12 offset:1024
	ds_read_b128 v[8:11], v12 offset:2048
	ds_read_b128 v[12:15], v12 offset:3072
	ds_read_b128 v[16:19], v28
	ds_read_b128 v[20:23], v28 offset:1024
	ds_read_b128 v[24:27], v28 offset:2048
	ds_read_b128 v[28:31], v28 offset:3072
	s_mov_b32 m0, s77
	v_lshl_add_u64 v[218:219], s[4:5], 0, v[218:219]
	ds_read_b128 v[32:35], v237 offset:32768
	ds_read_b128 v[36:39], v237 offset:33792
	ds_read_b128 v[40:43], v237 offset:34816
	ds_read_b128 v[44:47], v237 offset:35840
	ds_read_b128 v[48:51], v237 offset:36864
	ds_read_b128 v[52:55], v237 offset:37888
	ds_read_b128 v[56:59], v237 offset:38912
	ds_read_b128 v[60:63], v237 offset:39936
	global_load_lds_dwordx4 v[218:219], off
	v_lshl_add_u64 v[216:217], s[4:5], 0, v[216:217]
	s_mov_b32 m0, s80
	s_nop 0
	global_load_lds_dwordx4 v[216:217], off
	s_waitcnt vmcnt(8)
	s_waitcnt lgkmcnt(0)
	s_barrier
	s_setprio 1
	v_mfma_scale_f32_16x16x128_f8f6f4 v[188:191], v[0:7], v[32:39], v[188:191], v220, v221 op_sel_hi:[0,0,0]
	v_mfma_scale_f32_16x16x128_f8f6f4 v[184:187], v[8:15], v[32:39], v[184:187], v220, v221 op_sel_hi:[0,0,0]
	v_mfma_scale_f32_16x16x128_f8f6f4 v[172:175], v[0:7], v[40:47], v[172:175], v220, v221 op_sel_hi:[0,0,0]
	v_mfma_scale_f32_16x16x128_f8f6f4 v[168:171], v[8:15], v[40:47], v[168:171], v220, v221 op_sel_hi:[0,0,0]
	v_mfma_scale_f32_16x16x128_f8f6f4 v[156:159], v[0:7], v[48:55], v[156:159], v220, v221 op_sel_hi:[0,0,0]
	v_mfma_scale_f32_16x16x128_f8f6f4 v[152:155], v[8:15], v[48:55], v[152:155], v220, v221 op_sel_hi:[0,0,0]
	v_mfma_scale_f32_16x16x128_f8f6f4 v[140:143], v[0:7], v[56:63], v[140:143], v220, v221 op_sel_hi:[0,0,0]
	v_mfma_scale_f32_16x16x128_f8f6f4 v[136:139], v[8:15], v[56:63], v[136:139], v220, v221 op_sel_hi:[0,0,0]
	s_setprio 0
	s_setprio 1
	v_mfma_scale_f32_16x16x128_f8f6f4 v[180:183], v[16:23], v[32:39], v[180:183], v220, v221 op_sel_hi:[0,0,0]
	v_mfma_scale_f32_16x16x128_f8f6f4 v[176:179], v[24:31], v[32:39], v[176:179], v220, v221 op_sel_hi:[0,0,0]
	v_mfma_scale_f32_16x16x128_f8f6f4 v[164:167], v[16:23], v[40:47], v[164:167], v220, v221 op_sel_hi:[0,0,0]
	v_mfma_scale_f32_16x16x128_f8f6f4 v[160:163], v[24:31], v[40:47], v[160:163], v220, v221 op_sel_hi:[0,0,0]
	v_mfma_scale_f32_16x16x128_f8f6f4 v[148:151], v[16:23], v[48:55], v[148:151], v220, v221 op_sel_hi:[0,0,0]
	v_mfma_scale_f32_16x16x128_f8f6f4 v[144:147], v[24:31], v[48:55], v[144:147], v220, v221 op_sel_hi:[0,0,0]
	v_mfma_scale_f32_16x16x128_f8f6f4 v[132:135], v[16:23], v[56:63], v[132:135], v220, v221 op_sel_hi:[0,0,0]
	v_mfma_scale_f32_16x16x128_f8f6f4 v[128:131], v[24:31], v[56:63], v[128:131], v220, v221 op_sel_hi:[0,0,0]
	s_setprio 0
	s_barrier
	s_add_i32 s2, s2, s69
	v_lshl_add_u64 v[194:195], v[194:195], 0, s[26:27]
	s_mov_b32 m0, s2
	ds_read_b128 v[32:35], v237 offset:49152
	ds_read_b128 v[36:39], v237 offset:50176
	ds_read_b128 v[40:43], v237 offset:51200
	ds_read_b128 v[44:47], v237 offset:52224
	ds_read_b128 v[48:51], v237 offset:53248
	ds_read_b128 v[52:55], v237 offset:54272
	ds_read_b128 v[56:59], v237 offset:55296
	ds_read_b128 v[60:63], v237 offset:56320
	global_load_lds_dwordx4 v[194:195], off
	s_add_i32 m0, s2, 0x2000
	s_add_u32 s4, s66, 0x20080
	v_lshl_add_u64 v[194:195], v[196:197], 0, s[26:27]
	s_addc_u32 s5, s67, 0
	s_add_i32 s2, s12, s69
	global_load_lds_dwordx4 v[194:195], off
	v_lshl_add_u64 v[194:195], s[4:5], 0, v[202:203]
	s_mov_b32 m0, s2
	s_nop 0
	global_load_lds_dwordx4 v[194:195], off
	v_lshl_add_u64 v[194:195], s[4:5], 0, v[204:205]
	s_add_i32 m0, s2, 0x2000
	s_nop 0
	global_load_lds_dwordx4 v[194:195], off
	v_lshl_add_u64 v[194:195], v[198:199], 0, s[26:27]
	s_mov_b32 m0, s88
	s_nop 0
	global_load_lds_dwordx4 v[194:195], off
	v_lshl_add_u64 v[194:195], v[226:227], 0, s[26:27]
	s_mov_b32 m0, s89
	s_nop 0
	global_load_lds_dwordx4 v[194:195], off
	s_waitcnt vmcnt(8)
	s_waitcnt lgkmcnt(0)
	s_barrier
	s_setprio 1
	v_mfma_scale_f32_16x16x128_f8f6f4 v[124:127], v[0:7], v[32:39], v[124:127], v220, v221 op_sel_hi:[0,0,0]
	v_mfma_scale_f32_16x16x128_f8f6f4 v[120:123], v[8:15], v[32:39], v[120:123], v220, v221 op_sel_hi:[0,0,0]
	v_mfma_scale_f32_16x16x128_f8f6f4 v[108:111], v[0:7], v[40:47], v[108:111], v220, v221 op_sel_hi:[0,0,0]
	v_mfma_scale_f32_16x16x128_f8f6f4 v[104:107], v[8:15], v[40:47], v[104:107], v220, v221 op_sel_hi:[0,0,0]
	v_mfma_scale_f32_16x16x128_f8f6f4 v[92:95], v[0:7], v[48:55], v[92:95], v220, v221 op_sel_hi:[0,0,0]
	v_mfma_scale_f32_16x16x128_f8f6f4 v[88:91], v[8:15], v[48:55], v[88:91], v220, v221 op_sel_hi:[0,0,0]
	v_mfma_scale_f32_16x16x128_f8f6f4 v[72:75], v[0:7], v[56:63], v[72:75], v220, v221 op_sel_hi:[0,0,0]
	v_mfma_scale_f32_16x16x128_f8f6f4 v[76:79], v[8:15], v[56:63], v[76:79], v220, v221 op_sel_hi:[0,0,0]
	s_setprio 0
	s_setprio 1
	v_mfma_scale_f32_16x16x128_f8f6f4 v[116:119], v[16:23], v[32:39], v[116:119], v220, v221 op_sel_hi:[0,0,0]
	v_mfma_scale_f32_16x16x128_f8f6f4 v[112:115], v[24:31], v[32:39], v[112:115], v220, v221 op_sel_hi:[0,0,0]
	v_mfma_scale_f32_16x16x128_f8f6f4 v[100:103], v[16:23], v[40:47], v[100:103], v220, v221 op_sel_hi:[0,0,0]
	v_mfma_scale_f32_16x16x128_f8f6f4 v[96:99], v[24:31], v[40:47], v[96:99], v220, v221 op_sel_hi:[0,0,0]
	v_mfma_scale_f32_16x16x128_f8f6f4 v[84:87], v[16:23], v[48:55], v[84:87], v220, v221 op_sel_hi:[0,0,0]
	v_mfma_scale_f32_16x16x128_f8f6f4 v[80:83], v[24:31], v[48:55], v[80:83], v220, v221 op_sel_hi:[0,0,0]
	v_mfma_scale_f32_16x16x128_f8f6f4 v[64:67], v[16:23], v[56:63], v[64:67], v220, v221 op_sel_hi:[0,0,0]
	v_mfma_scale_f32_16x16x128_f8f6f4 v[68:71], v[24:31], v[56:63], v[68:71], v220, v221 op_sel_hi:[0,0,0]
	s_setprio 0
	s_barrier
	s_add_i32 s86, s86, 2
	s_add_u32 s64, s64, 0x100
	s_addc_u32 s65, s65, 0
	s_add_u32 s61, s61, 0x100
	s_addc_u32 s83, s83, 0
	s_cmp_gt_u32 s86, 5
	s_cbranch_scc1 .LBB0_1325
